# row-pair load overlap: P6 second row's loads issued right after the first row's (fresh address pair), plus early gate-block addresses
# speedup vs baseline: 1.0037x; 1.0037x over previous
.LBB0_2123:
	v_lshl_add_u64 v[28:29], s[44:45], 0, v[16:17]
	v_add_co_u32_e32 v4, vcc, 0x37a00000, v28
	s_add_i32 s0, s80, s8
	s_nop 0
	v_addc_co_u32_e32 v5, vcc, 0, v29, vcc
	global_load_dwordx2 v[62:63], v[4:5], off
	global_load_dwordx2 v[60:61], v[4:5], off offset:512
	global_load_dwordx2 v[48:49], v[4:5], off offset:1024
	s_waitcnt lgkmcnt(0)
	global_load_dwordx2 v[6:7], v[4:5], off offset:1536
	global_load_dwordx2 v[46:47], v[4:5], off offset:2048
	global_load_dwordx2 v[44:45], v[4:5], off offset:2560
	global_load_dwordx2 v[42:43], v[4:5], off offset:3072
	s_nop 0
	global_load_dwordx2 v[4:5], v[4:5], off offset:3584
	s_cmp_lt_i32 s0, s86
	s_cselect_b32 s48, s0, s8
	s_ashr_i32 s49, s48, 31
	s_lshl_b64 s[50:51], s[48:49], 12
	v_lshl_add_u64 v[218:219], v[8:9], 0, s[50:51]
	global_load_dwordx2 v[40:41], v[218:219], off
	global_load_dwordx2 v[38:39], v[218:219], off offset:512
	global_load_dwordx2 v[36:37], v[218:219], off offset:1024
	global_load_dwordx2 v[250:251], v[218:219], off offset:1536
	global_load_dwordx2 v[34:35], v[218:219], off offset:2048
	global_load_dwordx2 v[32:33], v[218:219], off offset:2560
	global_load_dwordx2 v[30:31], v[218:219], off offset:3072
	global_load_dwordx2 v[50:51], v[218:219], off offset:3584
	v_mov_b32_e32 v2, s81
	s_min_i32 s0, s8, 0x4000
	s_lshr_b32 s0, s0, 12
	s_mulk_i32 s0, 0x3000
	s_ashr_i32 s1, s0, 31
	s_lshl_b64 s[0:1], s[0:1], 2
	s_add_u32 s2, s6, s0
	s_addc_u32 s3, s7, s1
	s_min_i32 s0, s48, 0x4000
	s_lshr_b32 s0, s0, 12
	s_mulk_i32 s0, 0x3000
	s_ashr_i32 s1, s0, 31
	s_lshl_b64 s[0:1], s[0:1], 2
	s_add_u32 s0, s6, s0
	s_addc_u32 s1, s7, s1
	s_waitcnt vmcnt(15)
	v_and_b32_e32 v103, 0xffff0000, v63
	v_and_b32_e32 v101, 0xffff0000, v62
	v_lshlrev_b32_e32 v102, 16, v63
	s_waitcnt vmcnt(12)
	v_lshlrev_b32_e32 v25, 16, v6
	s_waitcnt vmcnt(8)
	v_lshlrev_b32_e32 v21, 16, v4
	v_and_b32_e32 v19, 0xffff0000, v4
	v_lshlrev_b32_e32 v58, 16, v5
	v_and_b32_e32 v59, 0xffff0000, v5
	v_and_b32_e32 v23, 0xffff0000, v6
	v_lshlrev_b32_e32 v26, 16, v7
	v_and_b32_e32 v27, 0xffff0000, v7
	ds_read_b64 v[64:65], v2
	v_mul_f32_e32 v2, v103, v103
	v_lshlrev_b32_e32 v100, 16, v62
	v_pk_fma_f32 v[62:63], v[102:103], v[102:103], v[2:3] op_sel_hi:[1,1,0]
	v_and_b32_e32 v99, 0xffff0000, v61
	v_and_b32_e32 v98, 0xffff0000, v60
	v_mul_f32_e32 v2, v101, v101
	v_lshlrev_b32_e32 v95, 16, v61
	v_lshlrev_b32_e32 v94, 16, v60
	v_pk_mul_f32 v[60:61], v[98:99], v[98:99]
	v_lshlrev_b32_e32 v90, 16, v48
	v_and_b32_e32 v91, 0xffff0000, v48
	v_lshlrev_b32_e32 v96, 16, v49
	v_and_b32_e32 v97, 0xffff0000, v49
	v_pk_fma_f32 v[48:49], v[100:101], v[100:101], v[2:3] op_sel_hi:[1,1,0]
	s_waitcnt lgkmcnt(0)
	v_readfirstlane_b32 s9, v64
	v_readfirstlane_b32 s12, v65
	v_pk_fma_f32 v[60:61], v[94:95], v[94:95], v[60:61]
	v_mov_b32_e32 v24, v48
	v_mov_b32_e32 v64, v62
	v_mov_b32_e32 v65, v25
	v_mul_f32_e32 v4, v23, v23
	v_pk_add_f32 v[48:49], v[48:49], v[62:63]
	v_pk_mul_f32 v[62:63], v[24:25], v[64:65]
	v_pk_add_f32 v[60:61], v[60:61], v[60:61] op_sel:[0,1] op_sel_hi:[1,0]
	v_mov_b32_e32 v49, v63
	v_mov_b32_e32 v61, v4
	v_mul_f32_e32 v2, v91, v91
	v_pk_add_f32 v[48:49], v[48:49], v[60:61]
	v_pk_fma_f32 v[60:61], v[90:91], v[90:91], v[2:3] op_sel_hi:[1,1,0]
	v_mul_f32_e32 v2, v97, v97
	v_mul_f32_e32 v18, v27, v27
	v_pk_fma_f32 v[62:63], v[96:97], v[96:97], v[2:3] op_sel_hi:[1,1,0]
	v_and_b32_e32 v107, 0xffff0000, v47
	v_mov_b32_e32 v63, v18
	v_and_b32_e32 v106, 0xffff0000, v46
	v_lshlrev_b32_e32 v105, 16, v47
	v_lshlrev_b32_e32 v104, 16, v46
	v_pk_mul_f32 v[46:47], v[106:107], v[106:107]
	v_and_b32_e32 v93, 0xffff0000, v45
	v_pk_fma_f32 v[46:47], v[104:105], v[104:105], v[46:47]
	v_and_b32_e32 v92, 0xffff0000, v44
	v_pk_add_f32 v[46:47], v[46:47], v[46:47] op_sel:[0,1] op_sel_hi:[1,0]
	v_lshlrev_b32_e32 v89, 16, v45
	v_lshlrev_b32_e32 v88, 16, v44
	v_pk_mul_f32 v[44:45], v[92:93], v[92:93]
	v_lshlrev_b32_e32 v78, 16, v42
	v_and_b32_e32 v79, 0xffff0000, v42
	v_lshlrev_b32_e32 v80, 16, v43
	v_and_b32_e32 v81, 0xffff0000, v43
	v_pk_fma_f32 v[44:45], v[88:89], v[88:89], v[44:45]
	v_mul_f32_e32 v2, v19, v19
	v_pk_add_f32 v[44:45], v[44:45], v[44:45] op_sel:[0,1] op_sel_hi:[1,0]
	s_add_u32 s52, s9, s46
	v_mov_b32_e32 v45, v2
	v_mul_f32_e32 v2, v79, v79
	s_addc_u32 s53, s12, s47
	s_add_u32 s58, s2, 0x6000
	v_mul_f32_e32 v4, v58, v58
	s_addc_u32 s59, s3, 0
	s_add_u32 s60, s2, 0x8000
	s_addc_u32 s61, s3, 0
	s_add_u32 s54, s0, 0x6000
	s_addc_u32 s55, s1, 0
	s_add_u32 s56, s0, 0x8000
	s_mov_b32 s0, 0x3a000000
	s_addc_u32 s57, s1, 0
	v_mov_b32_e32 v22, v25
	s_waitcnt vmcnt(7)
	v_and_b32_e32 v73, 0xffff0000, v41
	v_and_b32_e32 v71, 0xffff0000, v40
	v_lshlrev_b32_e32 v72, 16, v41
	s_waitcnt vmcnt(4)
	v_mov_b32_e32 v6, v250
	v_mov_b32_e32 v7, v251
	v_lshlrev_b32_e32 v55, 16, v6
	v_and_b32_e32 v53, 0xffff0000, v6
	v_mul_f32_e32 v6, v26, v26
	v_mov_b32_e32 v61, v6
	v_pk_add_f32 v[60:61], v[60:61], v[62:63]
	v_mul_f32_e32 v6, v59, v59
	v_pk_add_f32 v[48:49], v[48:49], v[60:61]
	v_lshlrev_b32_e32 v70, 16, v40
	v_pk_add_f32 v[42:43], v[48:49], v[48:49] op_sel:[0,1] op_sel_hi:[1,0]
	v_mov_b32_e32 v48, v46
	v_mov_b32_e32 v20, v42
	v_mov_b32_e32 v49, v21
	v_pk_add_f32 v[42:43], v[42:43], v[46:47]
	v_pk_mul_f32 v[46:47], v[20:21], v[48:49]
	v_and_b32_e32 v77, 0xffff0000, v39
	v_mov_b32_e32 v43, v47
	v_pk_add_f32 v[42:43], v[42:43], v[44:45]
	v_pk_fma_f32 v[44:45], v[78:79], v[78:79], v[2:3] op_sel_hi:[1,1,0]
	v_mul_f32_e32 v2, v81, v81
	v_pk_fma_f32 v[46:47], v[80:81], v[80:81], v[2:3] op_sel_hi:[1,1,0]
	v_mov_b32_e32 v45, v4
	v_mov_b32_e32 v47, v6
	v_pk_add_f32 v[44:45], v[44:45], v[46:47]
	v_mul_f32_e32 v2, v73, v73
	v_pk_add_f32 v[108:109], v[42:43], v[44:45]
	global_load_dwordx4 v[118:121], v181, s[52:53]
	global_load_dwordx4 v[122:125], v181, s[60:61]
	global_load_dwordx4 v[126:129], v181, s[58:59]
	global_load_dwordx4 v[130:133], v181, s[52:53] offset:1024
	global_load_dwordx4 v[134:137], v182, s[60:61]
	global_load_dwordx4 v[138:141], v182, s[58:59]
	global_load_dwordx4 v[142:145], v181, s[52:53] offset:2048
	global_load_dwordx4 v[146:149], v183, s[60:61]
	global_load_dwordx4 v[150:153], v183, s[58:59]
	global_load_dwordx4 v[154:157], v181, s[52:53] offset:3072
	global_load_dwordx4 v[158:161], v184, s[60:61]
	global_load_dwordx4 v[162:165], v184, s[58:59]
	global_load_dwordx4 v[166:169], v185, s[52:53]
	global_load_dwordx4 v[170:173], v185, s[60:61]
	global_load_dwordx4 v[174:177], v185, s[58:59]
	global_load_dwordx4 v[214:217], v186, s[52:53]
	global_load_dwordx4 v[224:227], v186, s[60:61]
	global_load_dwordx4 v[228:231], v186, s[58:59]
	global_load_dwordx4 v[232:235], v187, s[52:53]
	global_load_dwordx4 v[236:239], v187, s[60:61]
	global_load_dwordx4 v[240:243], v187, s[58:59]
	global_load_dwordx4 v[244:247], v190, s[52:53]
	global_load_dwordx4 v[248:251], v190, s[60:61]
	v_pk_fma_f32 v[40:41], v[72:73], v[72:73], v[2:3] op_sel_hi:[1,1,0]
	v_and_b32_e32 v76, 0xffff0000, v38
	v_mul_f32_e32 v2, v71, v71
	v_lshlrev_b32_e32 v75, 16, v39
	v_lshlrev_b32_e32 v74, 16, v38
	v_pk_mul_f32 v[38:39], v[76:77], v[76:77]
	v_lshlrev_b32_e32 v62, 16, v36
	v_and_b32_e32 v63, 0xffff0000, v36
	v_lshlrev_b32_e32 v64, 16, v37
	v_and_b32_e32 v65, 0xffff0000, v37
	v_pk_fma_f32 v[36:37], v[70:71], v[70:71], v[2:3] op_sel_hi:[1,1,0]
	v_pk_fma_f32 v[38:39], v[74:75], v[74:75], v[38:39]
	v_mov_b32_e32 v54, v36
	v_mul_f32_e32 v4, v53, v53
	v_pk_add_f32 v[36:37], v[36:37], v[40:41]
	v_pk_add_f32 v[38:39], v[38:39], v[38:39] op_sel:[0,1] op_sel_hi:[1,0]
	v_mul_f32_e32 v2, v63, v63
	v_mov_b32_e32 v39, v4
	v_lshlrev_b32_e32 v56, 16, v7
	v_and_b32_e32 v57, 0xffff0000, v7
	v_mul_f32_e32 v6, v56, v56
	v_mul_f32_e32 v18, v57, v57
	s_waitcnt vmcnt(26)
	v_and_b32_e32 v69, 0xffff0000, v35
	v_and_b32_e32 v68, 0xffff0000, v34
	v_lshlrev_b32_e32 v67, 16, v35
	v_lshlrev_b32_e32 v66, 16, v34
	v_pk_mul_f32 v[34:35], v[68:69], v[68:69]
	s_waitcnt vmcnt(25)
	v_and_b32_e32 v87, 0xffff0000, v33
	v_pk_fma_f32 v[34:35], v[66:67], v[66:67], v[34:35]
	v_and_b32_e32 v86, 0xffff0000, v32
	s_waitcnt vmcnt(23)
	v_lshlrev_b32_e32 v7, 16, v50
	v_pk_add_f32 v[34:35], v[34:35], v[34:35] op_sel:[0,1] op_sel_hi:[1,0]
	v_lshlrev_b32_e32 v61, 16, v33
	v_lshlrev_b32_e32 v60, 16, v32
	v_pk_mul_f32 v[32:33], v[86:87], v[86:87]
	v_lshlrev_b32_e32 v82, 16, v30
	v_and_b32_e32 v83, 0xffff0000, v30
	v_lshlrev_b32_e32 v84, 16, v31
	v_and_b32_e32 v85, 0xffff0000, v31
	v_and_b32_e32 v5, 0xffff0000, v50
	v_pk_fma_f32 v[32:33], v[60:61], v[60:61], v[32:33]
	v_lshlrev_b32_e32 v50, 16, v51
	v_pk_add_f32 v[32:33], v[32:33], v[32:33] op_sel:[0,1] op_sel_hi:[1,0]
	v_and_b32_e32 v51, 0xffff0000, v51
	v_mul_f32_e32 v4, v50, v50
	v_mov_b32_e32 v52, v55
	s_waitcnt vmcnt(21)
	v_mov_b32_e32 v42, v118
	v_mov_b32_e32 v43, v119
	v_mov_b32_e32 v44, v120
	v_mov_b32_e32 v45, v121
	v_mov_b32_e32 v46, v122
	v_mov_b32_e32 v47, v123
	v_mov_b32_e32 v48, v124
	v_mov_b32_e32 v49, v125
	global_load_dwordx4 v[118:121], v190, s[58:59]
	global_load_dwordx4 v[122:125], v181, s[52:53]
	v_pk_add_f32 v[212:213], v[46:47], 1.0 op_sel_hi:[1,0]
	v_mov_b32_e32 v46, v40
	v_mov_b32_e32 v47, v55
	v_pk_mul_f32 v[40:41], v[54:55], v[46:47]
	v_pk_add_f32 v[48:49], v[48:49], 1.0 op_sel_hi:[1,0]
	v_mov_b32_e32 v37, v41
	v_pk_add_f32 v[36:37], v[36:37], v[38:39]
	v_pk_fma_f32 v[38:39], v[62:63], v[62:63], v[2:3] op_sel_hi:[1,1,0]
	v_mul_f32_e32 v2, v65, v65
	v_pk_fma_f32 v[40:41], v[64:65], v[64:65], v[2:3] op_sel_hi:[1,1,0]
	v_mov_b32_e32 v39, v6
	v_mov_b32_e32 v41, v18
	v_pk_add_f32 v[38:39], v[38:39], v[40:41]
	v_mul_f32_e32 v2, v5, v5
	v_pk_add_f32 v[36:37], v[36:37], v[38:39]
	v_mov_b32_e32 v33, v2
	v_pk_add_f32 v[30:31], v[36:37], v[36:37] op_sel:[0,1] op_sel_hi:[1,0]
	v_mov_b32_e32 v36, v34
	v_mov_b32_e32 v6, v30
	v_mov_b32_e32 v37, v7
	v_pk_add_f32 v[30:31], v[30:31], v[34:35]
	v_pk_mul_f32 v[34:35], v[6:7], v[36:37]
	v_mul_f32_e32 v2, v83, v83
	v_mov_b32_e32 v31, v35
	v_pk_add_f32 v[30:31], v[30:31], v[32:33]
	v_pk_fma_f32 v[32:33], v[82:83], v[82:83], v[2:3] op_sel_hi:[1,1,0]
	v_mul_f32_e32 v2, v85, v85
	v_mul_f32_e32 v18, v51, v51
	v_pk_fma_f32 v[34:35], v[84:85], v[84:85], v[2:3] op_sel_hi:[1,1,0]
	v_mov_b32_e32 v33, v4
	v_mov_b32_e32 v35, v18
	v_pk_add_f32 v[32:33], v[32:33], v[34:35]
	v_mov_b32_e32 v40, v95
	v_pk_add_f32 v[30:31], v[30:31], v[32:33]
	v_mov_b32_e32 v33, v108
	v_mov_b32_e32 v32, v30
	v_mov_b32_e32 v108, v31
	v_pk_add_f32 v[30:31], v[32:33], v[108:109]
	v_mov_b32_e32 v41, v99
	v_mov_b32_e32 v95, v98
	v_mov_b32_dpp v33, v31 quad_perm:[1,0,3,2] row_mask:0xf bank_mask:0xf bound_ctrl:1
	v_mov_b32_dpp v32, v30 quad_perm:[1,0,3,2] row_mask:0xf bank_mask:0xf bound_ctrl:1
	v_pk_add_f32 v[30:31], v[30:31], v[32:33]
	v_mov_b32_e32 v18, v21
	s_nop 0
	v_mov_b32_dpp v33, v31 quad_perm:[2,3,0,1] row_mask:0xf bank_mask:0xf bound_ctrl:1
	v_mov_b32_dpp v32, v30 quad_perm:[2,3,0,1] row_mask:0xf bank_mask:0xf bound_ctrl:1
	v_pk_add_f32 v[30:31], v[30:31], v[32:33]
	s_nop 1
	v_mov_b32_dpp v33, v31 row_half_mirror row_mask:0xf bank_mask:0xf bound_ctrl:1
	v_mov_b32_dpp v32, v30 row_half_mirror row_mask:0xf bank_mask:0xf bound_ctrl:1
	v_pk_add_f32 v[30:31], v[30:31], v[32:33]
	s_nop 1
	v_mov_b32_dpp v33, v31 row_mirror row_mask:0xf bank_mask:0xf bound_ctrl:1
	v_mov_b32_dpp v32, v30 row_mirror row_mask:0xf bank_mask:0xf bound_ctrl:1
	v_pk_add_f32 v[30:31], v[30:31], v[32:33]
	ds_bpermute_b32 v33, v111, v31
	ds_bpermute_b32 v32, v111, v30
	s_waitcnt lgkmcnt(0)
	v_pk_add_f32 v[30:31], v[30:31], v[32:33]
	ds_bpermute_b32 v33, v112, v31
	ds_bpermute_b32 v32, v112, v30
	s_waitcnt lgkmcnt(0)
	v_pk_add_f32 v[30:31], v[30:31], v[32:33]
	s_nop 0
	v_pk_fma_f32 v[108:109], v[30:31], s[0:1], v[188:189] op_sel_hi:[1,0,0]
	s_nop 0
	v_mul_f32_e32 v2, 0x4b800000, v109
	v_cmp_gt_f32_e64 s[0:1], s11, v109
	v_cmp_gt_f32_e32 vcc, s11, v108
	s_nop 0
	v_cndmask_b32_e64 v2, v109, v2, s[0:1]
	v_rsq_f32_e32 v2, v2
	s_nop 0
	v_mul_f32_e32 v4, 0x45800000, v2
	v_cndmask_b32_e64 v2, v2, v4, s[0:1]
	v_pk_mul_f32 v[30:31], v[2:3], v[102:103] op_sel_hi:[0,1]
	v_pk_mul_f32 v[32:33], v[2:3], v[100:101] op_sel_hi:[0,1]
	v_pk_mul_f32 v[32:33], v[42:43], v[32:33]
	v_pk_mul_f32 v[30:31], v[44:45], v[30:31]
	s_mov_b32 s0, 0x40200000
	s_waitcnt vmcnt(22)
	v_mov_b32_e32 v192, v126
	v_mov_b32_e32 v193, v127
	v_mov_b32_e32 v194, v128
	v_mov_b32_e32 v195, v129
	global_load_dwordx4 v[126:129], v181, s[56:57]
	v_pk_fma_f32 v[46:47], v[48:49], v[30:31], v[194:195]
	v_pk_fma_f32 v[48:49], v[212:213], v[32:33], v[192:193]
	v_add_co_u32_e64 v100, s[0:1], s0, v28
	v_cvt_pk_bf16_f32 v30, v48, v49
	v_cvt_pk_bf16_f32 v31, v46, v47
	v_addc_co_u32_e64 v101, s[0:1], 0, v29, s[0:1]
	global_store_dwordx2 v[100:101], v[30:31], off
	s_nop 0
	v_pk_mul_f32 v[40:41], v[2:3], v[40:41] op_sel_hi:[0,1]
	v_pk_mul_f32 v[42:43], v[2:3], v[94:95] op_sel_hi:[0,1]
	v_pk_mul_f32 v[90:91], v[2:3], v[90:91] op_sel_hi:[0,1]
	v_pk_mul_f32 v[26:27], v[2:3], v[26:27] op_sel_hi:[0,1]
	v_pk_mul_f32 v[22:23], v[2:3], v[22:23] op_sel_hi:[0,1]
	v_pk_mul_f32 v[80:81], v[2:3], v[80:81] op_sel_hi:[0,1]
	v_pk_mul_f32 v[78:79], v[2:3], v[78:79] op_sel_hi:[0,1]
	v_pk_mul_f32 v[58:59], v[2:3], v[58:59] op_sel_hi:[0,1]
	v_pk_mul_f32 v[18:19], v[2:3], v[18:19] op_sel_hi:[0,1]
	s_waitcnt vmcnt(23)
	v_mov_b32_e32 v28, v130
	v_mov_b32_e32 v29, v131
	v_mov_b32_e32 v30, v132
	v_mov_b32_e32 v31, v133
	global_load_dwordx4 v[130:133], v181, s[54:55]
	v_pk_mul_f32 v[28:29], v[28:29], v[42:43]
	v_pk_mul_f32 v[30:31], v[30:31], v[40:41]
	s_waitcnt vmcnt(23)
	v_mov_b32_e32 v32, v134
	v_mov_b32_e32 v33, v135
	v_mov_b32_e32 v34, v136
	v_mov_b32_e32 v35, v137
	global_load_dwordx4 v[134:137], v181, s[52:53] offset:1024
	v_pk_add_f32 v[34:35], v[34:35], 1.0 op_sel_hi:[1,0]
	v_pk_add_f32 v[32:33], v[32:33], 1.0 op_sel_hi:[1,0]
	s_waitcnt vmcnt(23)
	v_mov_b32_e32 v36, v138
	v_mov_b32_e32 v37, v139
	v_mov_b32_e32 v38, v140
	v_mov_b32_e32 v39, v141
	global_load_dwordx4 v[138:141], v182, s[56:57]
	v_pk_fma_f32 v[42:43], v[34:35], v[30:31], v[38:39]
	v_pk_fma_f32 v[44:45], v[32:33], v[28:29], v[36:37]
	v_cvt_pk_bf16_f32 v29, v42, v43
	v_cvt_pk_bf16_f32 v28, v44, v45
	global_store_dwordx2 v[100:101], v[28:29], off offset:512
	s_nop 0
	v_pk_mul_f32 v[40:41], v[2:3], v[96:97] op_sel_hi:[0,1]
	s_waitcnt vmcnt(24)
	v_mov_b32_e32 v28, v142
	v_mov_b32_e32 v29, v143
	v_mov_b32_e32 v30, v144
	v_mov_b32_e32 v31, v145
	global_load_dwordx4 v[142:145], v182, s[54:55]
	v_pk_mul_f32 v[28:29], v[28:29], v[90:91]
	v_pk_mul_f32 v[30:31], v[30:31], v[40:41]
	s_waitcnt vmcnt(24)
	v_mov_b32_e32 v32, v146
	v_mov_b32_e32 v33, v147
	v_mov_b32_e32 v34, v148
	v_mov_b32_e32 v35, v149
	global_load_dwordx4 v[146:149], v181, s[52:53] offset:2048
	v_pk_add_f32 v[34:35], v[34:35], 1.0 op_sel_hi:[1,0]
	v_pk_add_f32 v[32:33], v[32:33], 1.0 op_sel_hi:[1,0]
	s_waitcnt vmcnt(24)
	v_mov_b32_e32 v36, v150
	v_mov_b32_e32 v37, v151
	v_mov_b32_e32 v38, v152
	v_mov_b32_e32 v39, v153
	global_load_dwordx4 v[150:153], v183, s[56:57]
	v_pk_fma_f32 v[38:39], v[34:35], v[30:31], v[38:39]
	v_pk_fma_f32 v[40:41], v[32:33], v[28:29], v[36:37]
	v_cvt_pk_bf16_f32 v29, v38, v39
	v_cvt_pk_bf16_f32 v28, v40, v41
	global_store_dwordx2 v[100:101], v[28:29], off offset:1024
	s_nop 0
	v_mov_b32_e32 v90, v89
	v_mov_b32_e32 v91, v93
	v_mov_b32_e32 v89, v92
	v_pk_mul_f32 v[90:91], v[2:3], v[90:91] op_sel_hi:[0,1]
	v_pk_mul_f32 v[88:89], v[2:3], v[88:89] op_sel_hi:[0,1]
	s_waitcnt vmcnt(25)
	v_mov_b32_e32 v28, v154
	v_mov_b32_e32 v29, v155
	v_mov_b32_e32 v30, v156
	v_mov_b32_e32 v31, v157
	global_load_dwordx4 v[154:157], v183, s[54:55]
	v_pk_mul_f32 v[22:23], v[22:23], v[28:29]
	v_pk_mul_f32 v[24:25], v[26:27], v[30:31]
	s_waitcnt vmcnt(25)
	v_mov_b32_e32 v32, v158
	v_mov_b32_e32 v33, v159
	v_mov_b32_e32 v34, v160
	v_mov_b32_e32 v35, v161
	global_load_dwordx4 v[158:161], v181, s[52:53] offset:3072
	v_pk_add_f32 v[26:27], v[34:35], 1.0 op_sel_hi:[1,0]
	v_pk_add_f32 v[28:29], v[32:33], 1.0 op_sel_hi:[1,0]
	s_waitcnt vmcnt(25)
	v_mov_b32_e32 v94, v162
	v_mov_b32_e32 v95, v163
	v_mov_b32_e32 v96, v164
	v_mov_b32_e32 v97, v165
	global_load_dwordx4 v[162:165], v184, s[56:57]
	v_pk_fma_f32 v[30:31], v[24:25], v[26:27], v[96:97]
	v_pk_fma_f32 v[32:33], v[22:23], v[28:29], v[94:95]
	v_cvt_pk_bf16_f32 v23, v30, v31
	v_cvt_pk_bf16_f32 v22, v32, v33
	global_store_dwordx2 v[100:101], v[22:23], off offset:1536
	s_nop 0
	v_mov_b32_e32 v34, v105
	v_mov_b32_e32 v35, v107
	v_mov_b32_e32 v105, v106
	v_pk_mul_f32 v[34:35], v[2:3], v[34:35] op_sel_hi:[0,1]
	v_pk_mul_f32 v[36:37], v[2:3], v[104:105] op_sel_hi:[0,1]
	v_mul_f32_e32 v2, 0x4b800000, v108
	v_cndmask_b32_e32 v2, v108, v2, vcc
	v_rsq_f32_e32 v2, v2
	s_waitcnt vmcnt(26)
	v_mov_b32_e32 v22, v166
	v_mov_b32_e32 v23, v167
	v_mov_b32_e32 v24, v168
	v_mov_b32_e32 v25, v169
	global_load_dwordx4 v[166:169], v184, s[54:55]
	v_pk_mul_f32 v[22:23], v[36:37], v[22:23]
	v_pk_mul_f32 v[24:25], v[34:35], v[24:25]
	s_waitcnt vmcnt(26)
	v_mov_b32_e32 v26, v170
	v_mov_b32_e32 v27, v171
	v_mov_b32_e32 v28, v172
	v_mov_b32_e32 v29, v173
	global_load_dwordx4 v[170:173], v185, s[52:53]
	v_pk_add_f32 v[28:29], v[28:29], 1.0 op_sel_hi:[1,0]
	v_pk_add_f32 v[26:27], v[26:27], 1.0 op_sel_hi:[1,0]
	s_waitcnt vmcnt(26)
	v_mov_b32_e32 v94, v174
	v_mov_b32_e32 v95, v175
	v_mov_b32_e32 v96, v176
	v_mov_b32_e32 v97, v177
	global_load_dwordx4 v[174:177], v185, s[56:57]
	v_pk_fma_f32 v[34:35], v[24:25], v[28:29], v[96:97]
	v_pk_fma_f32 v[36:37], v[22:23], v[26:27], v[94:95]
	v_cvt_pk_bf16_f32 v23, v34, v35
	v_cvt_pk_bf16_f32 v22, v36, v37
	global_store_dwordx2 v[100:101], v[22:23], off offset:2048
	s_nop 0
	v_mul_f32_e32 v4, 0x45800000, v2
	v_cndmask_b32_e32 v2, v2, v4, vcc
	v_pk_mul_f32 v[70:71], v[2:3], v[70:71] op_sel_hi:[0,1]
	v_pk_mul_f32 v[62:63], v[2:3], v[62:63] op_sel_hi:[0,1]
	v_pk_mul_f32 v[56:57], v[2:3], v[56:57] op_sel_hi:[0,1]
	v_pk_mul_f32 v[52:53], v[2:3], v[52:53] op_sel_hi:[0,1]
	v_pk_mul_f32 v[82:83], v[2:3], v[82:83] op_sel_hi:[0,1]
	v_mov_b32_e32 v4, v7
	v_pk_mul_f32 v[50:51], v[2:3], v[50:51] op_sel_hi:[0,1]
	v_pk_mul_f32 v[4:5], v[2:3], v[4:5] op_sel_hi:[0,1]
	s_waitcnt vmcnt(27)
	v_mov_b32_e32 v22, v214
	v_mov_b32_e32 v23, v215
	v_mov_b32_e32 v24, v216
	v_mov_b32_e32 v25, v217
	global_load_dwordx4 v[214:217], v185, s[54:55]
	v_pk_mul_f32 v[22:23], v[88:89], v[22:23]
	v_pk_mul_f32 v[24:25], v[90:91], v[24:25]
	s_waitcnt vmcnt(27)
	v_mov_b32_e32 v26, v224
	v_mov_b32_e32 v27, v225
	v_mov_b32_e32 v28, v226
	v_mov_b32_e32 v29, v227
	global_load_dwordx4 v[224:227], v186, s[52:53]
	v_pk_add_f32 v[28:29], v[28:29], 1.0 op_sel_hi:[1,0]
	v_pk_add_f32 v[88:89], v[26:27], 1.0 op_sel_hi:[1,0]
	s_waitcnt vmcnt(27)
	v_mov_b32_e32 v94, v228
	v_mov_b32_e32 v95, v229
	v_mov_b32_e32 v96, v230
	v_mov_b32_e32 v97, v231
	global_load_dwordx4 v[228:231], v186, s[56:57]
	v_pk_fma_f32 v[26:27], v[24:25], v[28:29], v[96:97]
	v_pk_fma_f32 v[28:29], v[22:23], v[88:89], v[94:95]
	v_cvt_pk_bf16_f32 v23, v26, v27
	v_cvt_pk_bf16_f32 v22, v28, v29
	global_store_dwordx2 v[100:101], v[22:23], off offset:2560
	s_nop 0
	v_lshl_add_u64 v[96:97], v[12:13], 0, s[50:51]
	s_waitcnt vmcnt(28)
	v_mov_b32_e32 v22, v232
	v_mov_b32_e32 v23, v233
	v_mov_b32_e32 v24, v234
	v_mov_b32_e32 v25, v235
	global_load_dwordx4 v[232:235], v186, s[54:55]
	v_pk_mul_f32 v[78:79], v[78:79], v[22:23]
	v_pk_mul_f32 v[22:23], v[80:81], v[24:25]
	s_waitcnt vmcnt(28)
	v_mov_b32_e32 v88, v236
	v_mov_b32_e32 v89, v237
	v_mov_b32_e32 v90, v238
	v_mov_b32_e32 v91, v239
	global_load_dwordx4 v[236:239], v187, s[52:53]
	v_pk_add_f32 v[24:25], v[90:91], 1.0 op_sel_hi:[1,0]
	v_pk_add_f32 v[80:81], v[88:89], 1.0 op_sel_hi:[1,0]
	s_waitcnt vmcnt(28)
	v_mov_b32_e32 v92, v240
	v_mov_b32_e32 v93, v241
	v_mov_b32_e32 v94, v242
	v_mov_b32_e32 v95, v243
	global_load_dwordx4 v[240:243], v187, s[56:57]
	v_pk_fma_f32 v[22:23], v[22:23], v[24:25], v[94:95]
	v_pk_fma_f32 v[24:25], v[78:79], v[80:81], v[92:93]
	v_cvt_pk_bf16_f32 v79, v22, v23
	v_cvt_pk_bf16_f32 v78, v24, v25
	global_store_dwordx2 v[100:101], v[78:79], off offset:3072
	s_nop 0
	s_waitcnt vmcnt(29)
	v_mov_b32_e32 v78, v244
	v_mov_b32_e32 v79, v245
	v_mov_b32_e32 v80, v246
	v_mov_b32_e32 v81, v247
	global_load_dwordx4 v[244:247], v187, s[54:55]
	v_pk_mul_f32 v[20:21], v[18:19], v[78:79]
	v_pk_mul_f32 v[18:19], v[58:59], v[80:81]
	s_waitcnt vmcnt(29)
	v_mov_b32_e32 v88, v248
	v_mov_b32_e32 v89, v249
	v_mov_b32_e32 v90, v250
	v_mov_b32_e32 v91, v251
	global_load_dwordx4 v[248:251], v190, s[52:53]
	v_pk_add_f32 v[58:59], v[90:91], 1.0 op_sel_hi:[1,0]
	v_pk_add_f32 v[78:79], v[88:89], 1.0 op_sel_hi:[1,0]
	s_waitcnt vmcnt(29)
	v_mov_b32_e32 v92, v118
	v_mov_b32_e32 v93, v119
	v_mov_b32_e32 v94, v120
	v_mov_b32_e32 v95, v121
	global_load_dwordx4 v[118:121], v190, s[56:57]
	v_pk_fma_f32 v[18:19], v[18:19], v[58:59], v[94:95]
	v_pk_fma_f32 v[20:21], v[20:21], v[78:79], v[92:93]
	v_cvt_pk_bf16_f32 v59, v18, v19
	v_cvt_pk_bf16_f32 v58, v20, v21
	global_store_dwordx2 v[100:101], v[58:59], off offset:3584
	v_pk_mul_f32 v[58:59], v[2:3], v[72:73] op_sel_hi:[0,1]
	s_waitcnt vmcnt(30)
	v_mov_b32_e32 v78, v122
	v_mov_b32_e32 v79, v123
	v_mov_b32_e32 v80, v124
	v_mov_b32_e32 v81, v125
	global_load_dwordx4 v[122:125], v190, s[54:55]
	v_pk_mul_f32 v[72:73], v[78:79], v[70:71]
	v_pk_mul_f32 v[58:59], v[80:81], v[58:59]
	s_waitcnt vmcnt(30)
	v_mov_b32_e32 v88, v126
	v_mov_b32_e32 v89, v127
	v_mov_b32_e32 v90, v128
	v_mov_b32_e32 v91, v129
	v_pk_add_f32 v[70:71], v[90:91], 1.0 op_sel_hi:[1,0]
	v_pk_add_f32 v[78:79], v[88:89], 1.0 op_sel_hi:[1,0]
	s_waitcnt vmcnt(28)
	v_mov_b32_e32 v92, v130
	v_mov_b32_e32 v93, v131
	v_mov_b32_e32 v94, v132
	v_mov_b32_e32 v95, v133
	v_pk_fma_f32 v[70:71], v[70:71], v[58:59], v[94:95]
	v_pk_fma_f32 v[72:73], v[78:79], v[72:73], v[92:93]
	v_cvt_pk_bf16_f32 v59, v70, v71
	v_cvt_pk_bf16_f32 v58, v72, v73
	global_store_dwordx2 v[96:97], v[58:59], off
	v_mov_b32_e32 v58, v75
	v_mov_b32_e32 v59, v77
	v_mov_b32_e32 v75, v76
	v_pk_mul_f32 v[58:59], v[2:3], v[58:59] op_sel_hi:[0,1]
	v_pk_mul_f32 v[74:75], v[2:3], v[74:75] op_sel_hi:[0,1]
	s_waitcnt vmcnt(28)
	v_mov_b32_e32 v78, v134
	v_mov_b32_e32 v79, v135
	v_mov_b32_e32 v80, v136
	v_mov_b32_e32 v81, v137
	v_pk_mul_f32 v[74:75], v[78:79], v[74:75]
	v_pk_mul_f32 v[58:59], v[80:81], v[58:59]
	s_waitcnt vmcnt(27)
	v_mov_b32_e32 v88, v138
	v_mov_b32_e32 v89, v139
	v_mov_b32_e32 v90, v140
	v_mov_b32_e32 v91, v141
	v_pk_add_f32 v[76:77], v[90:91], 1.0 op_sel_hi:[1,0]
	v_pk_add_f32 v[80:81], v[88:89], 1.0 op_sel_hi:[1,0]
	s_waitcnt vmcnt(25)
	v_mov_b32_e32 v92, v142
	v_mov_b32_e32 v93, v143
	v_mov_b32_e32 v94, v144
	v_mov_b32_e32 v95, v145
	v_pk_fma_f32 v[78:79], v[76:77], v[58:59], v[94:95]
	v_pk_fma_f32 v[80:81], v[80:81], v[74:75], v[92:93]
	v_cvt_pk_bf16_f32 v59, v78, v79
	v_cvt_pk_bf16_f32 v58, v80, v81
	global_store_dwordx2 v[96:97], v[58:59], off offset:512
	v_pk_mul_f32 v[58:59], v[2:3], v[64:65] op_sel_hi:[0,1]
	s_waitcnt vmcnt(25)
	v_mov_b32_e32 v74, v146
	v_mov_b32_e32 v75, v147
	v_mov_b32_e32 v76, v148
	v_mov_b32_e32 v77, v149
	v_pk_mul_f32 v[62:63], v[74:75], v[62:63]
	v_pk_mul_f32 v[58:59], v[76:77], v[58:59]
	s_waitcnt vmcnt(24)
	v_mov_b32_e32 v88, v150
	v_mov_b32_e32 v89, v151
	v_mov_b32_e32 v90, v152
	v_mov_b32_e32 v91, v153
	v_pk_add_f32 v[64:65], v[90:91], 1.0 op_sel_hi:[1,0]
	v_pk_add_f32 v[76:77], v[88:89], 1.0 op_sel_hi:[1,0]
	s_waitcnt vmcnt(22)
	v_mov_b32_e32 v92, v154
	v_mov_b32_e32 v93, v155
	v_mov_b32_e32 v94, v156
	v_mov_b32_e32 v95, v157
	v_pk_fma_f32 v[74:75], v[64:65], v[58:59], v[94:95]
	v_pk_fma_f32 v[76:77], v[76:77], v[62:63], v[92:93]
	v_cvt_pk_bf16_f32 v59, v74, v75
	v_cvt_pk_bf16_f32 v58, v76, v77
	global_store_dwordx2 v[96:97], v[58:59], off offset:1024
	s_waitcnt vmcnt(22)
	v_mov_b32_e32 v62, v158
	v_mov_b32_e32 v63, v159
	v_mov_b32_e32 v64, v160
	v_mov_b32_e32 v65, v161
	v_pk_mul_f32 v[52:53], v[52:53], v[62:63]
	v_pk_mul_f32 v[54:55], v[56:57], v[64:65]
	s_waitcnt vmcnt(21)
	v_mov_b32_e32 v88, v162
	v_mov_b32_e32 v89, v163
	v_mov_b32_e32 v90, v164
	v_mov_b32_e32 v91, v165
	v_pk_add_f32 v[56:57], v[90:91], 1.0 op_sel_hi:[1,0]
	v_pk_add_f32 v[58:59], v[88:89], 1.0 op_sel_hi:[1,0]
	s_waitcnt vmcnt(19)
	v_mov_b32_e32 v92, v166
	v_mov_b32_e32 v93, v167
	v_mov_b32_e32 v94, v168
	v_mov_b32_e32 v95, v169
	v_pk_fma_f32 v[62:63], v[54:55], v[56:57], v[94:95]
	v_pk_fma_f32 v[64:65], v[52:53], v[58:59], v[92:93]
	v_cvt_pk_bf16_f32 v53, v62, v63
	v_cvt_pk_bf16_f32 v52, v64, v65
	global_store_dwordx2 v[96:97], v[52:53], off offset:1536
	s_nop 0
	v_mov_b32_e32 v92, v67
	v_mov_b32_e32 v93, v69
	v_mov_b32_e32 v67, v68
	v_pk_mul_f32 v[92:93], v[2:3], v[92:93] op_sel_hi:[0,1]
	v_pk_mul_f32 v[66:67], v[2:3], v[66:67] op_sel_hi:[0,1]
	s_waitcnt vmcnt(19)
	v_mov_b32_e32 v52, v170
	v_mov_b32_e32 v53, v171
	v_mov_b32_e32 v54, v172
	v_mov_b32_e32 v55, v173
	v_pk_mul_f32 v[52:53], v[66:67], v[52:53]
	v_pk_mul_f32 v[54:55], v[92:93], v[54:55]
	s_waitcnt vmcnt(18)
	v_mov_b32_e32 v56, v174
	v_mov_b32_e32 v57, v175
	v_mov_b32_e32 v58, v176
	v_mov_b32_e32 v59, v177
	v_pk_add_f32 v[58:59], v[58:59], 1.0 op_sel_hi:[1,0]
	v_pk_add_f32 v[56:57], v[56:57], 1.0 op_sel_hi:[1,0]
	s_waitcnt vmcnt(16)
	v_mov_b32_e32 v88, v214
	v_mov_b32_e32 v89, v215
	v_mov_b32_e32 v90, v216
	v_mov_b32_e32 v91, v217
	v_pk_fma_f32 v[66:67], v[54:55], v[58:59], v[90:91]
	v_pk_fma_f32 v[68:69], v[52:53], v[56:57], v[88:89]
	v_cvt_pk_bf16_f32 v53, v66, v67
	v_cvt_pk_bf16_f32 v52, v68, v69
	global_store_dwordx2 v[96:97], v[52:53], off offset:2048
	s_nop 0
	v_mov_b32_e32 v92, v61
	v_mov_b32_e32 v93, v87
	v_mov_b32_e32 v61, v86
	v_pk_mul_f32 v[92:93], v[2:3], v[92:93] op_sel_hi:[0,1]
	v_pk_mul_f32 v[60:61], v[2:3], v[60:61] op_sel_hi:[0,1]
	s_waitcnt vmcnt(16)
	v_mov_b32_e32 v52, v224
	v_mov_b32_e32 v53, v225
	v_mov_b32_e32 v54, v226
	v_mov_b32_e32 v55, v227
	v_pk_mul_f32 v[52:53], v[60:61], v[52:53]
	v_pk_mul_f32 v[54:55], v[92:93], v[54:55]
	s_waitcnt vmcnt(15)
	v_mov_b32_e32 v56, v228
	v_mov_b32_e32 v57, v229
	v_mov_b32_e32 v58, v230
	v_mov_b32_e32 v59, v231
	v_pk_add_f32 v[58:59], v[58:59], 1.0 op_sel_hi:[1,0]
	v_pk_add_f32 v[56:57], v[56:57], 1.0 op_sel_hi:[1,0]
	s_waitcnt vmcnt(13)
	v_mov_b32_e32 v88, v232
	v_mov_b32_e32 v89, v233
	v_mov_b32_e32 v90, v234
	v_mov_b32_e32 v91, v235
	v_pk_fma_f32 v[58:59], v[54:55], v[58:59], v[90:91]
	v_pk_fma_f32 v[60:61], v[52:53], v[56:57], v[88:89]
	v_cvt_pk_bf16_f32 v53, v58, v59
	v_cvt_pk_bf16_f32 v52, v60, v61
	global_store_dwordx2 v[96:97], v[52:53], off offset:2560
	s_nop 0
	v_pk_mul_f32 v[56:57], v[2:3], v[84:85] op_sel_hi:[0,1]
	s_waitcnt vmcnt(13)
	v_mov_b32_e32 v52, v236
	v_mov_b32_e32 v53, v237
	v_mov_b32_e32 v54, v238
	v_mov_b32_e32 v55, v239
	v_pk_mul_f32 v[52:53], v[82:83], v[52:53]
	v_pk_mul_f32 v[54:55], v[56:57], v[54:55]
	s_waitcnt vmcnt(12)
	v_mov_b32_e32 v86, v240
	v_mov_b32_e32 v87, v241
	v_mov_b32_e32 v88, v242
	v_mov_b32_e32 v89, v243
	v_pk_add_f32 v[56:57], v[88:89], 1.0 op_sel_hi:[1,0]
	v_pk_add_f32 v[82:83], v[86:87], 1.0 op_sel_hi:[1,0]
	s_waitcnt vmcnt(10)
	v_mov_b32_e32 v90, v244
	v_mov_b32_e32 v91, v245
	v_mov_b32_e32 v92, v246
	v_mov_b32_e32 v93, v247
	v_pk_fma_f32 v[54:55], v[54:55], v[56:57], v[92:93]
	v_pk_fma_f32 v[56:57], v[52:53], v[82:83], v[90:91]
	v_cvt_pk_bf16_f32 v53, v54, v55
	v_cvt_pk_bf16_f32 v52, v56, v57
	global_store_dwordx2 v[96:97], v[52:53], off offset:3072
	s_waitcnt vmcnt(10)
	v_mov_b32_e32 v82, v248
	v_mov_b32_e32 v83, v249
	v_mov_b32_e32 v84, v250
	v_mov_b32_e32 v85, v251
	v_pk_mul_f32 v[4:5], v[4:5], v[82:83]
	v_pk_mul_f32 v[6:7], v[50:51], v[84:85]
	s_waitcnt vmcnt(9)
	v_mov_b32_e32 v86, v118
	v_mov_b32_e32 v87, v119
	v_mov_b32_e32 v88, v120
	v_mov_b32_e32 v89, v121
	v_pk_add_f32 v[50:51], v[88:89], 1.0 op_sel_hi:[1,0]
	v_pk_add_f32 v[52:53], v[86:87], 1.0 op_sel_hi:[1,0]
	s_waitcnt vmcnt(7)
	v_mov_b32_e32 v90, v122
	v_mov_b32_e32 v91, v123
	v_mov_b32_e32 v92, v124
	v_mov_b32_e32 v93, v125
	v_pk_fma_f32 v[50:51], v[6:7], v[50:51], v[92:93]
	v_pk_fma_f32 v[52:53], v[4:5], v[52:53], v[90:91]
	v_cvt_pk_bf16_f32 v5, v50, v51
	v_cvt_pk_bf16_f32 v4, v52, v53
	global_store_dwordx2 v[96:97], v[4:5], off offset:3584
	v_add_u32_e32 v118, 0x10400, v110
	v_add_u32_e32 v119, 0x10800, v110
	v_add_u32_e32 v120, 0x10c00, v110
	v_add_u32_e32 v121, 0x11000, v110
	v_add_u32_e32 v122, 0x11400, v110
	v_add_u32_e32 v123, 0x11800, v110
	v_add_u32_e32 v124, 0x11c00, v110
	v_add_u32_e32 v125, 0x12000, v110
	v_add_u32_e32 v126, 0x12400, v110
	v_add_u32_e32 v127, 0x12800, v110
	v_add_u32_e32 v128, 0x12c00, v110
	v_add_u32_e32 v129, 0x13000, v110
	v_add_u32_e32 v130, 0x13400, v110
	v_add_u32_e32 v131, 0x13800, v110
	v_add_u32_e32 v132, 0x13c00, v110
	v_add_u32_e32 v133, 0x14000, v110
	v_add_u32_e32 v134, 0x14400, v110
	v_add_u32_e32 v135, 0x14800, v110
	v_add_u32_e32 v136, 0x14c00, v110
	v_add_u32_e32 v137, 0x15000, v110
	v_add_u32_e32 v138, 0x15400, v110
	v_add_u32_e32 v139, 0x15800, v110
	v_add_u32_e32 v140, 0x15c00, v110
	v_add_u32_e32 v141, 0x16000, v110
	v_add_u32_e32 v142, 0x16400, v110
	v_add_u32_e32 v143, 0x16800, v110
	v_add_u32_e32 v144, 0x16c00, v110
	v_add_u32_e32 v145, 0x17000, v110
	v_add_u32_e32 v146, 0x17400, v110
	v_add_u32_e32 v147, 0x17800, v110
	v_add_u32_e32 v148, 0x17c00, v110
	v_add_u32_e32 v149, 0x18000, v110
	v_add_u32_e32 v150, 0x18400, v110
	v_add_u32_e32 v151, 0x18800, v110
	v_add_u32_e32 v152, 0x18c00, v110
	v_add_u32_e32 v153, 0x19000, v110
	v_add_u32_e32 v154, 0x19400, v110
	v_add_u32_e32 v155, 0x19800, v110
	v_add_u32_e32 v156, 0x19c00, v110
	v_add_u32_e32 v157, 0x1a000, v110
	v_add_u32_e32 v158, 0x1a400, v110
	v_add_u32_e32 v159, 0x1a800, v110
	v_add_u32_e32 v160, 0x1ac00, v110
	v_add_u32_e32 v161, 0x1b000, v110
	v_add_u32_e32 v162, 0x1b400, v110
	v_add_u32_e32 v163, 0x1b800, v110
	v_add_u32_e32 v164, 0x1bc00, v110
	v_add_u32_e32 v165, 0x1c000, v110
	v_add_u32_e32 v166, 0x1c400, v110
	v_add_u32_e32 v167, 0x1c800, v110
	v_add_u32_e32 v168, 0x1cc00, v110
	v_add_u32_e32 v169, 0x1d000, v110
	v_add_u32_e32 v170, 0x1d400, v110
	v_add_u32_e32 v171, 0x1d800, v110
	v_add_u32_e32 v172, 0x1dc00, v110
	v_add_u32_e32 v173, 0x1e000, v110
	v_add_u32_e32 v174, 0x1e400, v110
	v_add_u32_e32 v175, 0x1e800, v110
	v_add_u32_e32 v176, 0x1ec00, v110
	v_add_u32_e32 v177, 0x1f000, v110
	ds_read_b128 v[224:227], v110
	ds_read_b128 v[228:231], v110 offset:1024
	ds_read_b128 v[232:235], v110 offset:2048
	ds_read_b128 v[236:239], v110 offset:3072
	ds_read_b128 v[240:243], v110 offset:4096
	ds_read_b128 v[244:247], v110 offset:5120
	s_waitcnt lgkmcnt(5)
	v_pk_mul_f32 v[248:249], v[224:225], v[48:49]
	v_pk_mul_f32 v[250:251], v[224:225], v[72:73]
	v_pk_fma_f32 v[248:249], v[226:227], v[46:47], v[248:249]
	v_pk_fma_f32 v[250:251], v[226:227], v[70:71], v[250:251]
	ds_read_b128 v[224:227], v110 offset:6144
	s_waitcnt lgkmcnt(5)
	v_pk_fma_f32 v[248:249], v[228:229], v[44:45], v[248:249]
	v_pk_fma_f32 v[250:251], v[228:229], v[80:81], v[250:251]
	v_pk_fma_f32 v[248:249], v[230:231], v[42:43], v[248:249]
	v_pk_fma_f32 v[250:251], v[230:231], v[78:79], v[250:251]
	ds_read_b128 v[228:231], v110 offset:7168
	s_waitcnt lgkmcnt(5)
	v_pk_fma_f32 v[248:249], v[232:233], v[40:41], v[248:249]
	v_pk_fma_f32 v[250:251], v[232:233], v[76:77], v[250:251]
	v_pk_fma_f32 v[248:249], v[234:235], v[38:39], v[248:249]
	v_pk_fma_f32 v[250:251], v[234:235], v[74:75], v[250:251]
	ds_read_b128 v[232:235], v110 offset:8192
	s_waitcnt lgkmcnt(5)
	v_pk_fma_f32 v[248:249], v[236:237], v[32:33], v[248:249]
	v_pk_fma_f32 v[250:251], v[236:237], v[64:65], v[250:251]
	v_pk_fma_f32 v[248:249], v[238:239], v[30:31], v[248:249]
	v_pk_fma_f32 v[250:251], v[238:239], v[62:63], v[250:251]
	ds_read_b128 v[236:239], v110 offset:9216
	s_waitcnt lgkmcnt(5)
	v_pk_fma_f32 v[248:249], v[240:241], v[36:37], v[248:249]
	v_pk_fma_f32 v[250:251], v[240:241], v[68:69], v[250:251]
	v_pk_fma_f32 v[248:249], v[242:243], v[34:35], v[248:249]
	v_pk_fma_f32 v[250:251], v[242:243], v[66:67], v[250:251]
	ds_read_b128 v[240:243], v110 offset:10240
	s_waitcnt lgkmcnt(5)
	v_pk_fma_f32 v[248:249], v[244:245], v[28:29], v[248:249]
	v_pk_fma_f32 v[250:251], v[244:245], v[60:61], v[250:251]
	v_pk_fma_f32 v[248:249], v[246:247], v[26:27], v[248:249]
	v_pk_fma_f32 v[250:251], v[246:247], v[58:59], v[250:251]
	ds_read_b128 v[244:247], v110 offset:11264
	s_waitcnt lgkmcnt(5)
	v_pk_fma_f32 v[248:249], v[224:225], v[24:25], v[248:249]
	v_pk_fma_f32 v[250:251], v[224:225], v[56:57], v[250:251]
	v_pk_fma_f32 v[248:249], v[226:227], v[22:23], v[248:249]
	v_pk_fma_f32 v[250:251], v[226:227], v[54:55], v[250:251]
	ds_read_b128 v[224:227], v110 offset:12288
	s_waitcnt lgkmcnt(5)
	v_pk_fma_f32 v[248:249], v[228:229], v[20:21], v[248:249]
	v_pk_fma_f32 v[250:251], v[228:229], v[52:53], v[250:251]
	v_pk_fma_f32 v[248:249], v[230:231], v[18:19], v[248:249]
	v_pk_fma_f32 v[250:251], v[230:231], v[50:51], v[250:251]
	ds_read_b128 v[228:231], v110 offset:13312
	v_add_f32_e32 v2, v248, v249
	v_add_f32_e32 v82, v250, v251
	s_waitcnt lgkmcnt(5)
	v_pk_mul_f32 v[248:249], v[232:233], v[48:49]
	v_pk_mul_f32 v[250:251], v[232:233], v[72:73]
	v_pk_fma_f32 v[248:249], v[234:235], v[46:47], v[248:249]
	v_pk_fma_f32 v[250:251], v[234:235], v[70:71], v[250:251]
	ds_read_b128 v[232:235], v110 offset:14336
	s_waitcnt lgkmcnt(5)
	v_pk_fma_f32 v[248:249], v[236:237], v[44:45], v[248:249]
	v_pk_fma_f32 v[250:251], v[236:237], v[80:81], v[250:251]
	v_pk_fma_f32 v[248:249], v[238:239], v[42:43], v[248:249]
	v_pk_fma_f32 v[250:251], v[238:239], v[78:79], v[250:251]
	ds_read_b128 v[236:239], v110 offset:15360
	s_waitcnt lgkmcnt(5)
	v_pk_fma_f32 v[248:249], v[240:241], v[40:41], v[248:249]
	v_pk_fma_f32 v[250:251], v[240:241], v[76:77], v[250:251]
	v_pk_fma_f32 v[248:249], v[242:243], v[38:39], v[248:249]
	v_pk_fma_f32 v[250:251], v[242:243], v[74:75], v[250:251]
	ds_read_b128 v[240:243], v110 offset:16384
	s_waitcnt lgkmcnt(5)
	v_pk_fma_f32 v[248:249], v[244:245], v[32:33], v[248:249]
	v_pk_fma_f32 v[250:251], v[244:245], v[64:65], v[250:251]
	v_pk_fma_f32 v[248:249], v[246:247], v[30:31], v[248:249]
	v_pk_fma_f32 v[250:251], v[246:247], v[62:63], v[250:251]
	ds_read_b128 v[244:247], v110 offset:17408
	s_waitcnt lgkmcnt(5)
	v_pk_fma_f32 v[248:249], v[224:225], v[36:37], v[248:249]
	v_pk_fma_f32 v[250:251], v[224:225], v[68:69], v[250:251]
	v_pk_fma_f32 v[248:249], v[226:227], v[34:35], v[248:249]
	v_pk_fma_f32 v[250:251], v[226:227], v[66:67], v[250:251]
	ds_read_b128 v[224:227], v110 offset:18432
	s_waitcnt lgkmcnt(5)
	v_pk_fma_f32 v[248:249], v[228:229], v[28:29], v[248:249]
	v_pk_fma_f32 v[250:251], v[228:229], v[60:61], v[250:251]
	v_pk_fma_f32 v[248:249], v[230:231], v[26:27], v[248:249]
	v_pk_fma_f32 v[250:251], v[230:231], v[58:59], v[250:251]
	ds_read_b128 v[228:231], v110 offset:19456
	s_waitcnt lgkmcnt(5)
	v_pk_fma_f32 v[248:249], v[232:233], v[24:25], v[248:249]
	v_pk_fma_f32 v[250:251], v[232:233], v[56:57], v[250:251]
	v_pk_fma_f32 v[248:249], v[234:235], v[22:23], v[248:249]
	v_pk_fma_f32 v[250:251], v[234:235], v[54:55], v[250:251]
	ds_read_b128 v[232:235], v110 offset:20480
	s_waitcnt lgkmcnt(5)
	v_pk_fma_f32 v[248:249], v[236:237], v[20:21], v[248:249]
	v_pk_fma_f32 v[250:251], v[236:237], v[52:53], v[250:251]
	v_pk_fma_f32 v[248:249], v[238:239], v[18:19], v[248:249]
	v_pk_fma_f32 v[250:251], v[238:239], v[50:51], v[250:251]
	ds_read_b128 v[236:239], v110 offset:21504
	v_add_f32_e32 v83, v248, v249
	v_add_f32_e32 v84, v250, v251
	s_waitcnt lgkmcnt(5)
	v_pk_mul_f32 v[248:249], v[240:241], v[48:49]
	v_pk_mul_f32 v[250:251], v[240:241], v[72:73]
	v_pk_fma_f32 v[248:249], v[242:243], v[46:47], v[248:249]
	v_pk_fma_f32 v[250:251], v[242:243], v[70:71], v[250:251]
	ds_read_b128 v[240:243], v110 offset:22528
	s_waitcnt lgkmcnt(5)
	v_pk_fma_f32 v[248:249], v[244:245], v[44:45], v[248:249]
	v_pk_fma_f32 v[250:251], v[244:245], v[80:81], v[250:251]
	v_pk_fma_f32 v[248:249], v[246:247], v[42:43], v[248:249]
	v_pk_fma_f32 v[250:251], v[246:247], v[78:79], v[250:251]
	ds_read_b128 v[244:247], v110 offset:23552
	s_waitcnt lgkmcnt(5)
	v_pk_fma_f32 v[248:249], v[224:225], v[40:41], v[248:249]
	v_pk_fma_f32 v[250:251], v[224:225], v[76:77], v[250:251]
	v_pk_fma_f32 v[248:249], v[226:227], v[38:39], v[248:249]
	v_pk_fma_f32 v[250:251], v[226:227], v[74:75], v[250:251]
	ds_read_b128 v[224:227], v110 offset:24576
	s_waitcnt lgkmcnt(5)
	v_pk_fma_f32 v[248:249], v[228:229], v[32:33], v[248:249]
	v_pk_fma_f32 v[250:251], v[228:229], v[64:65], v[250:251]
	v_pk_fma_f32 v[248:249], v[230:231], v[30:31], v[248:249]
	v_pk_fma_f32 v[250:251], v[230:231], v[62:63], v[250:251]
	ds_read_b128 v[228:231], v110 offset:25600
	s_waitcnt lgkmcnt(5)
	v_pk_fma_f32 v[248:249], v[232:233], v[36:37], v[248:249]
	v_pk_fma_f32 v[250:251], v[232:233], v[68:69], v[250:251]
	v_pk_fma_f32 v[248:249], v[234:235], v[34:35], v[248:249]
	v_pk_fma_f32 v[250:251], v[234:235], v[66:67], v[250:251]
	ds_read_b128 v[232:235], v110 offset:26624
	s_waitcnt lgkmcnt(5)
	v_pk_fma_f32 v[248:249], v[236:237], v[28:29], v[248:249]
	v_pk_fma_f32 v[250:251], v[236:237], v[60:61], v[250:251]
	v_pk_fma_f32 v[248:249], v[238:239], v[26:27], v[248:249]
	v_pk_fma_f32 v[250:251], v[238:239], v[58:59], v[250:251]
	ds_read_b128 v[236:239], v110 offset:27648
	s_waitcnt lgkmcnt(5)
	v_pk_fma_f32 v[248:249], v[240:241], v[24:25], v[248:249]
	v_pk_fma_f32 v[250:251], v[240:241], v[56:57], v[250:251]
	v_pk_fma_f32 v[248:249], v[242:243], v[22:23], v[248:249]
	v_pk_fma_f32 v[250:251], v[242:243], v[54:55], v[250:251]
	ds_read_b128 v[240:243], v110 offset:28672
	s_waitcnt lgkmcnt(5)
	v_pk_fma_f32 v[248:249], v[244:245], v[20:21], v[248:249]
	v_pk_fma_f32 v[250:251], v[244:245], v[52:53], v[250:251]
	v_pk_fma_f32 v[248:249], v[246:247], v[18:19], v[248:249]
	v_pk_fma_f32 v[250:251], v[246:247], v[50:51], v[250:251]
	ds_read_b128 v[244:247], v110 offset:29696
	v_add_f32_e32 v85, v248, v249
	v_add_f32_e32 v86, v250, v251
	s_waitcnt lgkmcnt(5)
	v_pk_mul_f32 v[248:249], v[224:225], v[48:49]
	v_pk_mul_f32 v[250:251], v[224:225], v[72:73]
	v_pk_fma_f32 v[248:249], v[226:227], v[46:47], v[248:249]
	v_pk_fma_f32 v[250:251], v[226:227], v[70:71], v[250:251]
	ds_read_b128 v[224:227], v110 offset:30720
	s_waitcnt lgkmcnt(5)
	v_pk_fma_f32 v[248:249], v[228:229], v[44:45], v[248:249]
	v_pk_fma_f32 v[250:251], v[228:229], v[80:81], v[250:251]
	v_pk_fma_f32 v[248:249], v[230:231], v[42:43], v[248:249]
	v_pk_fma_f32 v[250:251], v[230:231], v[78:79], v[250:251]
	ds_read_b128 v[228:231], v110 offset:31744
	s_waitcnt lgkmcnt(5)
	v_pk_fma_f32 v[248:249], v[232:233], v[40:41], v[248:249]
	v_pk_fma_f32 v[250:251], v[232:233], v[76:77], v[250:251]
	v_pk_fma_f32 v[248:249], v[234:235], v[38:39], v[248:249]
	v_pk_fma_f32 v[250:251], v[234:235], v[74:75], v[250:251]
	ds_read_b128 v[232:235], v110 offset:32768
	s_waitcnt lgkmcnt(5)
	v_pk_fma_f32 v[248:249], v[236:237], v[32:33], v[248:249]
	v_pk_fma_f32 v[250:251], v[236:237], v[64:65], v[250:251]
	v_pk_fma_f32 v[248:249], v[238:239], v[30:31], v[248:249]
	v_pk_fma_f32 v[250:251], v[238:239], v[62:63], v[250:251]
	ds_read_b128 v[236:239], v110 offset:33792
	s_waitcnt lgkmcnt(5)
	v_pk_fma_f32 v[248:249], v[240:241], v[36:37], v[248:249]
	v_pk_fma_f32 v[250:251], v[240:241], v[68:69], v[250:251]
	v_pk_fma_f32 v[248:249], v[242:243], v[34:35], v[248:249]
	v_pk_fma_f32 v[250:251], v[242:243], v[66:67], v[250:251]
	ds_read_b128 v[240:243], v110 offset:34816
	s_waitcnt lgkmcnt(5)
	v_pk_fma_f32 v[248:249], v[244:245], v[28:29], v[248:249]
	v_pk_fma_f32 v[250:251], v[244:245], v[60:61], v[250:251]
	v_pk_fma_f32 v[248:249], v[246:247], v[26:27], v[248:249]
	v_pk_fma_f32 v[250:251], v[246:247], v[58:59], v[250:251]
	ds_read_b128 v[244:247], v110 offset:35840
	s_waitcnt lgkmcnt(5)
	v_pk_fma_f32 v[248:249], v[224:225], v[24:25], v[248:249]
	v_pk_fma_f32 v[250:251], v[224:225], v[56:57], v[250:251]
	v_pk_fma_f32 v[248:249], v[226:227], v[22:23], v[248:249]
	v_pk_fma_f32 v[250:251], v[226:227], v[54:55], v[250:251]
	ds_read_b128 v[224:227], v110 offset:36864
	s_waitcnt lgkmcnt(5)
	v_pk_fma_f32 v[248:249], v[228:229], v[20:21], v[248:249]
	v_pk_fma_f32 v[250:251], v[228:229], v[52:53], v[250:251]
	v_pk_fma_f32 v[248:249], v[230:231], v[18:19], v[248:249]
	v_pk_fma_f32 v[250:251], v[230:231], v[50:51], v[250:251]
	ds_read_b128 v[228:231], v110 offset:37888
	v_add_f32_e32 v87, v248, v249
	v_add_f32_e32 v88, v250, v251
	s_waitcnt lgkmcnt(5)
	v_pk_mul_f32 v[248:249], v[232:233], v[48:49]
	v_pk_mul_f32 v[250:251], v[232:233], v[72:73]
	v_pk_fma_f32 v[248:249], v[234:235], v[46:47], v[248:249]
	v_pk_fma_f32 v[250:251], v[234:235], v[70:71], v[250:251]
	ds_read_b128 v[232:235], v110 offset:38912
	s_waitcnt lgkmcnt(5)
	v_pk_fma_f32 v[248:249], v[236:237], v[44:45], v[248:249]
	v_pk_fma_f32 v[250:251], v[236:237], v[80:81], v[250:251]
	v_pk_fma_f32 v[248:249], v[238:239], v[42:43], v[248:249]
	v_pk_fma_f32 v[250:251], v[238:239], v[78:79], v[250:251]
	ds_read_b128 v[236:239], v110 offset:39936
	s_waitcnt lgkmcnt(5)
	v_pk_fma_f32 v[248:249], v[240:241], v[40:41], v[248:249]
	v_pk_fma_f32 v[250:251], v[240:241], v[76:77], v[250:251]
	v_pk_fma_f32 v[248:249], v[242:243], v[38:39], v[248:249]
	v_pk_fma_f32 v[250:251], v[242:243], v[74:75], v[250:251]
	ds_read_b128 v[240:243], v110 offset:40960
	s_waitcnt lgkmcnt(5)
	v_pk_fma_f32 v[248:249], v[244:245], v[32:33], v[248:249]
	v_pk_fma_f32 v[250:251], v[244:245], v[64:65], v[250:251]
	v_pk_fma_f32 v[248:249], v[246:247], v[30:31], v[248:249]
	v_pk_fma_f32 v[250:251], v[246:247], v[62:63], v[250:251]
	ds_read_b128 v[244:247], v110 offset:41984
	s_waitcnt lgkmcnt(5)
	v_pk_fma_f32 v[248:249], v[224:225], v[36:37], v[248:249]
	v_pk_fma_f32 v[250:251], v[224:225], v[68:69], v[250:251]
	v_pk_fma_f32 v[248:249], v[226:227], v[34:35], v[248:249]
	v_pk_fma_f32 v[250:251], v[226:227], v[66:67], v[250:251]
	ds_read_b128 v[224:227], v110 offset:43008
	s_waitcnt lgkmcnt(5)
	v_pk_fma_f32 v[248:249], v[228:229], v[28:29], v[248:249]
	v_pk_fma_f32 v[250:251], v[228:229], v[60:61], v[250:251]
	v_pk_fma_f32 v[248:249], v[230:231], v[26:27], v[248:249]
	v_pk_fma_f32 v[250:251], v[230:231], v[58:59], v[250:251]
	ds_read_b128 v[228:231], v110 offset:44032
	s_waitcnt lgkmcnt(5)
	v_pk_fma_f32 v[248:249], v[232:233], v[24:25], v[248:249]
	v_pk_fma_f32 v[250:251], v[232:233], v[56:57], v[250:251]
	v_pk_fma_f32 v[248:249], v[234:235], v[22:23], v[248:249]
	v_pk_fma_f32 v[250:251], v[234:235], v[54:55], v[250:251]
	ds_read_b128 v[232:235], v110 offset:45056
	s_waitcnt lgkmcnt(5)
	v_pk_fma_f32 v[248:249], v[236:237], v[20:21], v[248:249]
	v_pk_fma_f32 v[250:251], v[236:237], v[52:53], v[250:251]
	v_pk_fma_f32 v[248:249], v[238:239], v[18:19], v[248:249]
	v_pk_fma_f32 v[250:251], v[238:239], v[50:51], v[250:251]
	ds_read_b128 v[236:239], v110 offset:46080
	v_add_f32_e32 v89, v248, v249
	v_add_f32_e32 v90, v250, v251
	s_waitcnt lgkmcnt(5)
	v_pk_mul_f32 v[248:249], v[240:241], v[48:49]
	v_pk_mul_f32 v[250:251], v[240:241], v[72:73]
	v_pk_fma_f32 v[248:249], v[242:243], v[46:47], v[248:249]
	v_pk_fma_f32 v[250:251], v[242:243], v[70:71], v[250:251]
	ds_read_b128 v[240:243], v110 offset:47104
	s_waitcnt lgkmcnt(5)
	v_pk_fma_f32 v[248:249], v[244:245], v[44:45], v[248:249]
	v_pk_fma_f32 v[250:251], v[244:245], v[80:81], v[250:251]
	v_pk_fma_f32 v[248:249], v[246:247], v[42:43], v[248:249]
	v_pk_fma_f32 v[250:251], v[246:247], v[78:79], v[250:251]
	ds_read_b128 v[244:247], v110 offset:48128
	s_waitcnt lgkmcnt(5)
	v_pk_fma_f32 v[248:249], v[224:225], v[40:41], v[248:249]
	v_pk_fma_f32 v[250:251], v[224:225], v[76:77], v[250:251]
	v_pk_fma_f32 v[248:249], v[226:227], v[38:39], v[248:249]
	v_pk_fma_f32 v[250:251], v[226:227], v[74:75], v[250:251]
	ds_read_b128 v[224:227], v110 offset:49152
	s_waitcnt lgkmcnt(5)
	v_pk_fma_f32 v[248:249], v[228:229], v[32:33], v[248:249]
	v_pk_fma_f32 v[250:251], v[228:229], v[64:65], v[250:251]
	v_pk_fma_f32 v[248:249], v[230:231], v[30:31], v[248:249]
	v_pk_fma_f32 v[250:251], v[230:231], v[62:63], v[250:251]
	ds_read_b128 v[228:231], v110 offset:50176
	s_waitcnt lgkmcnt(5)
	v_pk_fma_f32 v[248:249], v[232:233], v[36:37], v[248:249]
	v_pk_fma_f32 v[250:251], v[232:233], v[68:69], v[250:251]
	v_pk_fma_f32 v[248:249], v[234:235], v[34:35], v[248:249]
	v_pk_fma_f32 v[250:251], v[234:235], v[66:67], v[250:251]
	ds_read_b128 v[232:235], v110 offset:51200
	s_waitcnt lgkmcnt(5)
	v_pk_fma_f32 v[248:249], v[236:237], v[28:29], v[248:249]
	v_pk_fma_f32 v[250:251], v[236:237], v[60:61], v[250:251]
	v_pk_fma_f32 v[248:249], v[238:239], v[26:27], v[248:249]
	v_pk_fma_f32 v[250:251], v[238:239], v[58:59], v[250:251]
	ds_read_b128 v[236:239], v110 offset:52224
	s_waitcnt lgkmcnt(5)
	v_pk_fma_f32 v[248:249], v[240:241], v[24:25], v[248:249]
	v_pk_fma_f32 v[250:251], v[240:241], v[56:57], v[250:251]
	v_pk_fma_f32 v[248:249], v[242:243], v[22:23], v[248:249]
	v_pk_fma_f32 v[250:251], v[242:243], v[54:55], v[250:251]
	ds_read_b128 v[240:243], v110 offset:53248
	s_waitcnt lgkmcnt(5)
	v_pk_fma_f32 v[248:249], v[244:245], v[20:21], v[248:249]
	v_pk_fma_f32 v[250:251], v[244:245], v[52:53], v[250:251]
	v_pk_fma_f32 v[248:249], v[246:247], v[18:19], v[248:249]
	v_pk_fma_f32 v[250:251], v[246:247], v[50:51], v[250:251]
	ds_read_b128 v[244:247], v110 offset:54272
	v_add_f32_e32 v91, v248, v249
	v_add_f32_e32 v92, v250, v251
	s_waitcnt lgkmcnt(5)
	v_pk_mul_f32 v[248:249], v[224:225], v[48:49]
	v_pk_mul_f32 v[250:251], v[224:225], v[72:73]
	v_pk_fma_f32 v[248:249], v[226:227], v[46:47], v[248:249]
	v_pk_fma_f32 v[250:251], v[226:227], v[70:71], v[250:251]
	ds_read_b128 v[224:227], v110 offset:55296
	s_waitcnt lgkmcnt(5)
	v_pk_fma_f32 v[248:249], v[228:229], v[44:45], v[248:249]
	v_pk_fma_f32 v[250:251], v[228:229], v[80:81], v[250:251]
	v_pk_fma_f32 v[248:249], v[230:231], v[42:43], v[248:249]
	v_pk_fma_f32 v[250:251], v[230:231], v[78:79], v[250:251]
	ds_read_b128 v[228:231], v110 offset:56320
	s_waitcnt lgkmcnt(5)
	v_pk_fma_f32 v[248:249], v[232:233], v[40:41], v[248:249]
	v_pk_fma_f32 v[250:251], v[232:233], v[76:77], v[250:251]
	v_pk_fma_f32 v[248:249], v[234:235], v[38:39], v[248:249]
	v_pk_fma_f32 v[250:251], v[234:235], v[74:75], v[250:251]
	ds_read_b128 v[232:235], v110 offset:57344
	s_waitcnt lgkmcnt(5)
	v_pk_fma_f32 v[248:249], v[236:237], v[32:33], v[248:249]
	v_pk_fma_f32 v[250:251], v[236:237], v[64:65], v[250:251]
	v_pk_fma_f32 v[248:249], v[238:239], v[30:31], v[248:249]
	v_pk_fma_f32 v[250:251], v[238:239], v[62:63], v[250:251]
	ds_read_b128 v[236:239], v110 offset:58368
	s_waitcnt lgkmcnt(5)
	v_pk_fma_f32 v[248:249], v[240:241], v[36:37], v[248:249]
	v_pk_fma_f32 v[250:251], v[240:241], v[68:69], v[250:251]
	v_pk_fma_f32 v[248:249], v[242:243], v[34:35], v[248:249]
	v_pk_fma_f32 v[250:251], v[242:243], v[66:67], v[250:251]
	ds_read_b128 v[240:243], v110 offset:59392
	s_waitcnt lgkmcnt(5)
	v_pk_fma_f32 v[248:249], v[244:245], v[28:29], v[248:249]
	v_pk_fma_f32 v[250:251], v[244:245], v[60:61], v[250:251]
	v_pk_fma_f32 v[248:249], v[246:247], v[26:27], v[248:249]
	v_pk_fma_f32 v[250:251], v[246:247], v[58:59], v[250:251]
	ds_read_b128 v[244:247], v110 offset:60416
	s_waitcnt lgkmcnt(5)
	v_pk_fma_f32 v[248:249], v[224:225], v[24:25], v[248:249]
	v_pk_fma_f32 v[250:251], v[224:225], v[56:57], v[250:251]
	v_pk_fma_f32 v[248:249], v[226:227], v[22:23], v[248:249]
	v_pk_fma_f32 v[250:251], v[226:227], v[54:55], v[250:251]
	ds_read_b128 v[224:227], v110 offset:61440
	s_waitcnt lgkmcnt(5)
	v_pk_fma_f32 v[248:249], v[228:229], v[20:21], v[248:249]
	v_pk_fma_f32 v[250:251], v[228:229], v[52:53], v[250:251]
	v_pk_fma_f32 v[248:249], v[230:231], v[18:19], v[248:249]
	v_pk_fma_f32 v[250:251], v[230:231], v[50:51], v[250:251]
	ds_read_b128 v[228:231], v110 offset:62464
	v_add_f32_e32 v93, v248, v249
	v_add_f32_e32 v94, v250, v251
	s_waitcnt lgkmcnt(5)
	v_pk_mul_f32 v[248:249], v[232:233], v[48:49]
	v_pk_mul_f32 v[250:251], v[232:233], v[72:73]
	v_pk_fma_f32 v[248:249], v[234:235], v[46:47], v[248:249]
	v_pk_fma_f32 v[250:251], v[234:235], v[70:71], v[250:251]
	ds_read_b128 v[232:235], v110 offset:63488
	s_waitcnt lgkmcnt(5)
	v_pk_fma_f32 v[248:249], v[236:237], v[44:45], v[248:249]
	v_pk_fma_f32 v[250:251], v[236:237], v[80:81], v[250:251]
	v_pk_fma_f32 v[248:249], v[238:239], v[42:43], v[248:249]
	v_pk_fma_f32 v[250:251], v[238:239], v[78:79], v[250:251]
	ds_read_b128 v[236:239], v110 offset:64512
	s_waitcnt lgkmcnt(5)
	v_pk_fma_f32 v[248:249], v[240:241], v[40:41], v[248:249]
	v_pk_fma_f32 v[250:251], v[240:241], v[76:77], v[250:251]
	v_pk_fma_f32 v[248:249], v[242:243], v[38:39], v[248:249]
	v_pk_fma_f32 v[250:251], v[242:243], v[74:75], v[250:251]
	ds_read_b128 v[240:243], v117
	s_waitcnt lgkmcnt(5)
	v_pk_fma_f32 v[248:249], v[244:245], v[32:33], v[248:249]
	v_pk_fma_f32 v[250:251], v[244:245], v[64:65], v[250:251]
	v_pk_fma_f32 v[248:249], v[246:247], v[30:31], v[248:249]
	v_pk_fma_f32 v[250:251], v[246:247], v[62:63], v[250:251]
	ds_read_b128 v[244:247], v118
	s_waitcnt lgkmcnt(5)
	v_pk_fma_f32 v[248:249], v[224:225], v[36:37], v[248:249]
	v_pk_fma_f32 v[250:251], v[224:225], v[68:69], v[250:251]
	v_pk_fma_f32 v[248:249], v[226:227], v[34:35], v[248:249]
	v_pk_fma_f32 v[250:251], v[226:227], v[66:67], v[250:251]
	ds_read_b128 v[224:227], v119
	s_waitcnt lgkmcnt(5)
	v_pk_fma_f32 v[248:249], v[228:229], v[28:29], v[248:249]
	v_pk_fma_f32 v[250:251], v[228:229], v[60:61], v[250:251]
	v_pk_fma_f32 v[248:249], v[230:231], v[26:27], v[248:249]
	v_pk_fma_f32 v[250:251], v[230:231], v[58:59], v[250:251]
	ds_read_b128 v[228:231], v120
	s_waitcnt lgkmcnt(5)
	v_pk_fma_f32 v[248:249], v[232:233], v[24:25], v[248:249]
	v_pk_fma_f32 v[250:251], v[232:233], v[56:57], v[250:251]
	v_pk_fma_f32 v[248:249], v[234:235], v[22:23], v[248:249]
	v_pk_fma_f32 v[250:251], v[234:235], v[54:55], v[250:251]
	ds_read_b128 v[232:235], v121
	s_waitcnt lgkmcnt(5)
	v_pk_fma_f32 v[248:249], v[236:237], v[20:21], v[248:249]
	v_pk_fma_f32 v[250:251], v[236:237], v[52:53], v[250:251]
	v_pk_fma_f32 v[248:249], v[238:239], v[18:19], v[248:249]
	v_pk_fma_f32 v[250:251], v[238:239], v[50:51], v[250:251]
	ds_read_b128 v[236:239], v122
	v_add_f32_e32 v95, v248, v249
	v_add_f32_e32 v96, v250, v251
	s_waitcnt lgkmcnt(5)
	v_pk_mul_f32 v[248:249], v[240:241], v[48:49]
	v_pk_mul_f32 v[250:251], v[240:241], v[72:73]
	v_pk_fma_f32 v[248:249], v[242:243], v[46:47], v[248:249]
	v_pk_fma_f32 v[250:251], v[242:243], v[70:71], v[250:251]
	ds_read_b128 v[240:243], v123
	s_waitcnt lgkmcnt(5)
	v_pk_fma_f32 v[248:249], v[244:245], v[44:45], v[248:249]
	v_pk_fma_f32 v[250:251], v[244:245], v[80:81], v[250:251]
	v_pk_fma_f32 v[248:249], v[246:247], v[42:43], v[248:249]
	v_pk_fma_f32 v[250:251], v[246:247], v[78:79], v[250:251]
	ds_read_b128 v[244:247], v124
	s_waitcnt lgkmcnt(5)
	v_pk_fma_f32 v[248:249], v[224:225], v[40:41], v[248:249]
	v_pk_fma_f32 v[250:251], v[224:225], v[76:77], v[250:251]
	v_pk_fma_f32 v[248:249], v[226:227], v[38:39], v[248:249]
	v_pk_fma_f32 v[250:251], v[226:227], v[74:75], v[250:251]
	ds_read_b128 v[224:227], v125
	s_waitcnt lgkmcnt(5)
	v_pk_fma_f32 v[248:249], v[228:229], v[32:33], v[248:249]
	v_pk_fma_f32 v[250:251], v[228:229], v[64:65], v[250:251]
	v_pk_fma_f32 v[248:249], v[230:231], v[30:31], v[248:249]
	v_pk_fma_f32 v[250:251], v[230:231], v[62:63], v[250:251]
	ds_read_b128 v[228:231], v126
	s_waitcnt lgkmcnt(5)
	v_pk_fma_f32 v[248:249], v[232:233], v[36:37], v[248:249]
	v_pk_fma_f32 v[250:251], v[232:233], v[68:69], v[250:251]
	v_pk_fma_f32 v[248:249], v[234:235], v[34:35], v[248:249]
	v_pk_fma_f32 v[250:251], v[234:235], v[66:67], v[250:251]
	ds_read_b128 v[232:235], v127
	s_waitcnt lgkmcnt(5)
	v_pk_fma_f32 v[248:249], v[236:237], v[28:29], v[248:249]
	v_pk_fma_f32 v[250:251], v[236:237], v[60:61], v[250:251]
	v_pk_fma_f32 v[248:249], v[238:239], v[26:27], v[248:249]
	v_pk_fma_f32 v[250:251], v[238:239], v[58:59], v[250:251]
	ds_read_b128 v[236:239], v128
	s_waitcnt lgkmcnt(5)
	v_pk_fma_f32 v[248:249], v[240:241], v[24:25], v[248:249]
	v_pk_fma_f32 v[250:251], v[240:241], v[56:57], v[250:251]
	v_pk_fma_f32 v[248:249], v[242:243], v[22:23], v[248:249]
	v_pk_fma_f32 v[250:251], v[242:243], v[54:55], v[250:251]
	ds_read_b128 v[240:243], v129
	s_waitcnt lgkmcnt(5)
	v_pk_fma_f32 v[248:249], v[244:245], v[20:21], v[248:249]
	v_pk_fma_f32 v[250:251], v[244:245], v[52:53], v[250:251]
	v_pk_fma_f32 v[248:249], v[246:247], v[18:19], v[248:249]
	v_pk_fma_f32 v[250:251], v[246:247], v[50:51], v[250:251]
	ds_read_b128 v[244:247], v130
	v_add_f32_e32 v4, v248, v249
	v_add_f32_e32 v5, v250, v251
	s_waitcnt lgkmcnt(5)
	v_pk_mul_f32 v[248:249], v[224:225], v[48:49]
	v_pk_mul_f32 v[250:251], v[224:225], v[72:73]
	v_pk_fma_f32 v[248:249], v[226:227], v[46:47], v[248:249]
	v_pk_fma_f32 v[250:251], v[226:227], v[70:71], v[250:251]
	ds_read_b128 v[224:227], v131
	s_waitcnt lgkmcnt(5)
	v_pk_fma_f32 v[248:249], v[228:229], v[44:45], v[248:249]
	v_pk_fma_f32 v[250:251], v[228:229], v[80:81], v[250:251]
	v_pk_fma_f32 v[248:249], v[230:231], v[42:43], v[248:249]
	v_pk_fma_f32 v[250:251], v[230:231], v[78:79], v[250:251]
	ds_read_b128 v[228:231], v132
	s_waitcnt lgkmcnt(5)
	v_pk_fma_f32 v[248:249], v[232:233], v[40:41], v[248:249]
	v_pk_fma_f32 v[250:251], v[232:233], v[76:77], v[250:251]
	v_pk_fma_f32 v[248:249], v[234:235], v[38:39], v[248:249]
	v_pk_fma_f32 v[250:251], v[234:235], v[74:75], v[250:251]
	ds_read_b128 v[232:235], v133
	s_waitcnt lgkmcnt(5)
	v_pk_fma_f32 v[248:249], v[236:237], v[32:33], v[248:249]
	v_pk_fma_f32 v[250:251], v[236:237], v[64:65], v[250:251]
	v_pk_fma_f32 v[248:249], v[238:239], v[30:31], v[248:249]
	v_pk_fma_f32 v[250:251], v[238:239], v[62:63], v[250:251]
	ds_read_b128 v[236:239], v134
	s_waitcnt lgkmcnt(5)
	v_pk_fma_f32 v[248:249], v[240:241], v[36:37], v[248:249]
	v_pk_fma_f32 v[250:251], v[240:241], v[68:69], v[250:251]
	v_pk_fma_f32 v[248:249], v[242:243], v[34:35], v[248:249]
	v_pk_fma_f32 v[250:251], v[242:243], v[66:67], v[250:251]
	ds_read_b128 v[240:243], v135
	s_waitcnt lgkmcnt(5)
	v_pk_fma_f32 v[248:249], v[244:245], v[28:29], v[248:249]
	v_pk_fma_f32 v[250:251], v[244:245], v[60:61], v[250:251]
	v_pk_fma_f32 v[248:249], v[246:247], v[26:27], v[248:249]
	v_pk_fma_f32 v[250:251], v[246:247], v[58:59], v[250:251]
	ds_read_b128 v[244:247], v136
	s_waitcnt lgkmcnt(5)
	v_pk_fma_f32 v[248:249], v[224:225], v[24:25], v[248:249]
	v_pk_fma_f32 v[250:251], v[224:225], v[56:57], v[250:251]
	v_pk_fma_f32 v[248:249], v[226:227], v[22:23], v[248:249]
	v_pk_fma_f32 v[250:251], v[226:227], v[54:55], v[250:251]
	ds_read_b128 v[224:227], v137
	s_waitcnt lgkmcnt(5)
	v_pk_fma_f32 v[248:249], v[228:229], v[20:21], v[248:249]
	v_pk_fma_f32 v[250:251], v[228:229], v[52:53], v[250:251]
	v_pk_fma_f32 v[248:249], v[230:231], v[18:19], v[248:249]
	v_pk_fma_f32 v[250:251], v[230:231], v[50:51], v[250:251]
	ds_read_b128 v[228:231], v138
	v_add_f32_e32 v6, v248, v249
	v_add_f32_e32 v7, v250, v251
	s_waitcnt lgkmcnt(5)
	v_pk_mul_f32 v[248:249], v[232:233], v[48:49]
	v_pk_mul_f32 v[250:251], v[232:233], v[72:73]
	v_pk_fma_f32 v[248:249], v[234:235], v[46:47], v[248:249]
	v_pk_fma_f32 v[250:251], v[234:235], v[70:71], v[250:251]
	ds_read_b128 v[232:235], v139
	s_waitcnt lgkmcnt(5)
	v_pk_fma_f32 v[248:249], v[236:237], v[44:45], v[248:249]
	v_pk_fma_f32 v[250:251], v[236:237], v[80:81], v[250:251]
	v_pk_fma_f32 v[248:249], v[238:239], v[42:43], v[248:249]
	v_pk_fma_f32 v[250:251], v[238:239], v[78:79], v[250:251]
	ds_read_b128 v[236:239], v140
	s_waitcnt lgkmcnt(5)
	v_pk_fma_f32 v[248:249], v[240:241], v[40:41], v[248:249]
	v_pk_fma_f32 v[250:251], v[240:241], v[76:77], v[250:251]
	v_pk_fma_f32 v[248:249], v[242:243], v[38:39], v[248:249]
	v_pk_fma_f32 v[250:251], v[242:243], v[74:75], v[250:251]
	ds_read_b128 v[240:243], v141
	s_waitcnt lgkmcnt(5)
	v_pk_fma_f32 v[248:249], v[244:245], v[32:33], v[248:249]
	v_pk_fma_f32 v[250:251], v[244:245], v[64:65], v[250:251]
	v_pk_fma_f32 v[248:249], v[246:247], v[30:31], v[248:249]
	v_pk_fma_f32 v[250:251], v[246:247], v[62:63], v[250:251]
	ds_read_b128 v[244:247], v142
	s_waitcnt lgkmcnt(5)
	v_pk_fma_f32 v[248:249], v[224:225], v[36:37], v[248:249]
	v_pk_fma_f32 v[250:251], v[224:225], v[68:69], v[250:251]
	v_pk_fma_f32 v[248:249], v[226:227], v[34:35], v[248:249]
	v_pk_fma_f32 v[250:251], v[226:227], v[66:67], v[250:251]
	ds_read_b128 v[224:227], v143
	s_waitcnt lgkmcnt(5)
	v_pk_fma_f32 v[248:249], v[228:229], v[28:29], v[248:249]
	v_pk_fma_f32 v[250:251], v[228:229], v[60:61], v[250:251]
	v_pk_fma_f32 v[248:249], v[230:231], v[26:27], v[248:249]
	v_pk_fma_f32 v[250:251], v[230:231], v[58:59], v[250:251]
	ds_read_b128 v[228:231], v144
	s_waitcnt lgkmcnt(5)
	v_pk_fma_f32 v[248:249], v[232:233], v[24:25], v[248:249]
	v_pk_fma_f32 v[250:251], v[232:233], v[56:57], v[250:251]
	v_pk_fma_f32 v[248:249], v[234:235], v[22:23], v[248:249]
	v_pk_fma_f32 v[250:251], v[234:235], v[54:55], v[250:251]
	ds_read_b128 v[232:235], v145
	s_waitcnt lgkmcnt(5)
	v_pk_fma_f32 v[248:249], v[236:237], v[20:21], v[248:249]
	v_pk_fma_f32 v[250:251], v[236:237], v[52:53], v[250:251]
	v_pk_fma_f32 v[248:249], v[238:239], v[18:19], v[248:249]
	v_pk_fma_f32 v[250:251], v[238:239], v[50:51], v[250:251]
	ds_read_b128 v[236:239], v146
	v_add_f32_e32 v97, v248, v249
	v_add_f32_e32 v98, v250, v251
	s_waitcnt lgkmcnt(5)
	v_pk_mul_f32 v[248:249], v[240:241], v[48:49]
	v_pk_mul_f32 v[250:251], v[240:241], v[72:73]
	v_pk_fma_f32 v[248:249], v[242:243], v[46:47], v[248:249]
	v_pk_fma_f32 v[250:251], v[242:243], v[70:71], v[250:251]
	ds_read_b128 v[240:243], v147
	s_waitcnt lgkmcnt(5)
	v_pk_fma_f32 v[248:249], v[244:245], v[44:45], v[248:249]
	v_pk_fma_f32 v[250:251], v[244:245], v[80:81], v[250:251]
	v_pk_fma_f32 v[248:249], v[246:247], v[42:43], v[248:249]
	v_pk_fma_f32 v[250:251], v[246:247], v[78:79], v[250:251]
	ds_read_b128 v[244:247], v148
	s_waitcnt lgkmcnt(5)
	v_pk_fma_f32 v[248:249], v[224:225], v[40:41], v[248:249]
	v_pk_fma_f32 v[250:251], v[224:225], v[76:77], v[250:251]
	v_pk_fma_f32 v[248:249], v[226:227], v[38:39], v[248:249]
	v_pk_fma_f32 v[250:251], v[226:227], v[74:75], v[250:251]
	ds_read_b128 v[224:227], v149
	s_waitcnt lgkmcnt(5)
	v_pk_fma_f32 v[248:249], v[228:229], v[32:33], v[248:249]
	v_pk_fma_f32 v[250:251], v[228:229], v[64:65], v[250:251]
	v_pk_fma_f32 v[248:249], v[230:231], v[30:31], v[248:249]
	v_pk_fma_f32 v[250:251], v[230:231], v[62:63], v[250:251]
	ds_read_b128 v[228:231], v150
	s_waitcnt lgkmcnt(5)
	v_pk_fma_f32 v[248:249], v[232:233], v[36:37], v[248:249]
	v_pk_fma_f32 v[250:251], v[232:233], v[68:69], v[250:251]
	v_pk_fma_f32 v[248:249], v[234:235], v[34:35], v[248:249]
	v_pk_fma_f32 v[250:251], v[234:235], v[66:67], v[250:251]
	ds_read_b128 v[232:235], v151
	s_waitcnt lgkmcnt(5)
	v_pk_fma_f32 v[248:249], v[236:237], v[28:29], v[248:249]
	v_pk_fma_f32 v[250:251], v[236:237], v[60:61], v[250:251]
	v_pk_fma_f32 v[248:249], v[238:239], v[26:27], v[248:249]
	v_pk_fma_f32 v[250:251], v[238:239], v[58:59], v[250:251]
	ds_read_b128 v[236:239], v152
	s_waitcnt lgkmcnt(5)
	v_pk_fma_f32 v[248:249], v[240:241], v[24:25], v[248:249]
	v_pk_fma_f32 v[250:251], v[240:241], v[56:57], v[250:251]
	v_pk_fma_f32 v[248:249], v[242:243], v[22:23], v[248:249]
	v_pk_fma_f32 v[250:251], v[242:243], v[54:55], v[250:251]
	ds_read_b128 v[240:243], v153
	s_waitcnt lgkmcnt(5)
	v_pk_fma_f32 v[248:249], v[244:245], v[20:21], v[248:249]
	v_pk_fma_f32 v[250:251], v[244:245], v[52:53], v[250:251]
	v_pk_fma_f32 v[248:249], v[246:247], v[18:19], v[248:249]
	v_pk_fma_f32 v[250:251], v[246:247], v[50:51], v[250:251]
	ds_read_b128 v[244:247], v154
	v_add_f32_e32 v99, v248, v249
	v_add_f32_e32 v100, v250, v251
	s_waitcnt lgkmcnt(5)
	v_pk_mul_f32 v[248:249], v[224:225], v[48:49]
	v_pk_mul_f32 v[250:251], v[224:225], v[72:73]
	v_pk_fma_f32 v[248:249], v[226:227], v[46:47], v[248:249]
	v_pk_fma_f32 v[250:251], v[226:227], v[70:71], v[250:251]
	ds_read_b128 v[224:227], v155
	s_waitcnt lgkmcnt(5)
	v_pk_fma_f32 v[248:249], v[228:229], v[44:45], v[248:249]
	v_pk_fma_f32 v[250:251], v[228:229], v[80:81], v[250:251]
	v_pk_fma_f32 v[248:249], v[230:231], v[42:43], v[248:249]
	v_pk_fma_f32 v[250:251], v[230:231], v[78:79], v[250:251]
	ds_read_b128 v[228:231], v156
	s_waitcnt lgkmcnt(5)
	v_pk_fma_f32 v[248:249], v[232:233], v[40:41], v[248:249]
	v_pk_fma_f32 v[250:251], v[232:233], v[76:77], v[250:251]
	v_pk_fma_f32 v[248:249], v[234:235], v[38:39], v[248:249]
	v_pk_fma_f32 v[250:251], v[234:235], v[74:75], v[250:251]
	ds_read_b128 v[232:235], v157
	s_waitcnt lgkmcnt(5)
	v_pk_fma_f32 v[248:249], v[236:237], v[32:33], v[248:249]
	v_pk_fma_f32 v[250:251], v[236:237], v[64:65], v[250:251]
	v_pk_fma_f32 v[248:249], v[238:239], v[30:31], v[248:249]
	v_pk_fma_f32 v[250:251], v[238:239], v[62:63], v[250:251]
	ds_read_b128 v[236:239], v158
	s_waitcnt lgkmcnt(5)
	v_pk_fma_f32 v[248:249], v[240:241], v[36:37], v[248:249]
	v_pk_fma_f32 v[250:251], v[240:241], v[68:69], v[250:251]
	v_pk_fma_f32 v[248:249], v[242:243], v[34:35], v[248:249]
	v_pk_fma_f32 v[250:251], v[242:243], v[66:67], v[250:251]
	ds_read_b128 v[240:243], v159
	s_waitcnt lgkmcnt(5)
	v_pk_fma_f32 v[248:249], v[244:245], v[28:29], v[248:249]
	v_pk_fma_f32 v[250:251], v[244:245], v[60:61], v[250:251]
	v_pk_fma_f32 v[248:249], v[246:247], v[26:27], v[248:249]
	v_pk_fma_f32 v[250:251], v[246:247], v[58:59], v[250:251]
	ds_read_b128 v[244:247], v160
	s_waitcnt lgkmcnt(5)
	v_pk_fma_f32 v[248:249], v[224:225], v[24:25], v[248:249]
	v_pk_fma_f32 v[250:251], v[224:225], v[56:57], v[250:251]
	v_pk_fma_f32 v[248:249], v[226:227], v[22:23], v[248:249]
	v_pk_fma_f32 v[250:251], v[226:227], v[54:55], v[250:251]
	ds_read_b128 v[224:227], v161
	s_waitcnt lgkmcnt(5)
	v_pk_fma_f32 v[248:249], v[228:229], v[20:21], v[248:249]
	v_pk_fma_f32 v[250:251], v[228:229], v[52:53], v[250:251]
	v_pk_fma_f32 v[248:249], v[230:231], v[18:19], v[248:249]
	v_pk_fma_f32 v[250:251], v[230:231], v[50:51], v[250:251]
	ds_read_b128 v[228:231], v162
	v_add_f32_e32 v101, v248, v249
	v_add_f32_e32 v102, v250, v251
	s_waitcnt lgkmcnt(5)
	v_pk_mul_f32 v[248:249], v[232:233], v[48:49]
	v_pk_mul_f32 v[250:251], v[232:233], v[72:73]
	v_pk_fma_f32 v[248:249], v[234:235], v[46:47], v[248:249]
	v_pk_fma_f32 v[250:251], v[234:235], v[70:71], v[250:251]
	ds_read_b128 v[232:235], v163
	s_waitcnt lgkmcnt(5)
	v_pk_fma_f32 v[248:249], v[236:237], v[44:45], v[248:249]
	v_pk_fma_f32 v[250:251], v[236:237], v[80:81], v[250:251]
	v_pk_fma_f32 v[248:249], v[238:239], v[42:43], v[248:249]
	v_pk_fma_f32 v[250:251], v[238:239], v[78:79], v[250:251]
	ds_read_b128 v[236:239], v164
	s_waitcnt lgkmcnt(5)
	v_pk_fma_f32 v[248:249], v[240:241], v[40:41], v[248:249]
	v_pk_fma_f32 v[250:251], v[240:241], v[76:77], v[250:251]
	v_pk_fma_f32 v[248:249], v[242:243], v[38:39], v[248:249]
	v_pk_fma_f32 v[250:251], v[242:243], v[74:75], v[250:251]
	s_waitcnt lgkmcnt(4)
	v_pk_fma_f32 v[248:249], v[244:245], v[32:33], v[248:249]
	v_pk_fma_f32 v[250:251], v[244:245], v[64:65], v[250:251]
	v_pk_fma_f32 v[248:249], v[246:247], v[30:31], v[248:249]
	v_pk_fma_f32 v[250:251], v[246:247], v[62:63], v[250:251]
	s_waitcnt lgkmcnt(3)
	v_pk_fma_f32 v[248:249], v[224:225], v[36:37], v[248:249]
	v_pk_fma_f32 v[250:251], v[224:225], v[68:69], v[250:251]
	v_pk_fma_f32 v[248:249], v[226:227], v[34:35], v[248:249]
	v_pk_fma_f32 v[250:251], v[226:227], v[66:67], v[250:251]
	s_waitcnt lgkmcnt(2)
	v_pk_fma_f32 v[248:249], v[228:229], v[28:29], v[248:249]
	v_pk_fma_f32 v[250:251], v[228:229], v[60:61], v[250:251]
	v_pk_fma_f32 v[248:249], v[230:231], v[26:27], v[248:249]
	v_pk_fma_f32 v[250:251], v[230:231], v[58:59], v[250:251]
	s_waitcnt lgkmcnt(1)
	v_pk_fma_f32 v[248:249], v[232:233], v[24:25], v[248:249]
	v_pk_fma_f32 v[250:251], v[232:233], v[56:57], v[250:251]
	v_pk_fma_f32 v[248:249], v[234:235], v[22:23], v[248:249]
	v_pk_fma_f32 v[250:251], v[234:235], v[54:55], v[250:251]
	s_waitcnt lgkmcnt(0)
	v_pk_fma_f32 v[248:249], v[236:237], v[20:21], v[248:249]
	v_pk_fma_f32 v[250:251], v[236:237], v[52:53], v[250:251]
	v_pk_fma_f32 v[248:249], v[238:239], v[18:19], v[248:249]
	v_pk_fma_f32 v[250:251], v[238:239], v[50:51], v[250:251]
	v_add_f32_e32 v103, v248, v249
	v_add_f32_e32 v104, v250, v251
	ds_read_b128 v[224:227], v165
	ds_read_b128 v[106:109], v166
	ds_read_b128 v[240:243], v167
	ds_read_b128 v[236:239], v168
	ds_read_b128 v[232:235], v169
	ds_read_b128 v[228:231], v170
	s_waitcnt lgkmcnt(5)
	v_mul_f32_e32 v105, v225, v49
	v_mul_f32_e32 v225, v225, v73
	v_fmac_f32_e32 v105, v224, v48
	v_fmac_f32_e32 v225, v224, v72
	v_mul_f32_e32 v224, v227, v71
	v_mul_f32_e32 v191, v227, v47
	v_fmac_f32_e32 v224, v226, v70
	v_fmac_f32_e32 v191, v226, v46
	v_add_f32_e32 v224, v225, v224
	v_add_f32_e32 v105, v105, v191
	v_add_f32_e32 v191, 0, v224
	ds_read_b128 v[224:227], v171
	v_add_f32_e32 v105, 0, v105
	s_waitcnt lgkmcnt(5)
	v_mul_f32_e32 v192, v107, v45
	v_mul_f32_e32 v107, v107, v81
	v_fmac_f32_e32 v192, v106, v44
	v_fmac_f32_e32 v107, v106, v80
	v_mul_f32_e32 v106, v109, v79
	v_fmac_f32_e32 v106, v108, v78
	v_mul_f32_e32 v193, v109, v43
	v_add_f32_e32 v106, v107, v106
	v_fmac_f32_e32 v193, v108, v42
	v_add_f32_e32 v191, v191, v106
	ds_read_b128 v[106:109], v172
	v_add_f32_e32 v192, v192, v193
	v_add_f32_e32 v105, v105, v192
	s_waitcnt lgkmcnt(5)
	v_mul_f32_e32 v192, v241, v41
	v_mul_f32_e32 v241, v241, v77
	v_fmac_f32_e32 v192, v240, v40
	v_fmac_f32_e32 v241, v240, v76
	v_mul_f32_e32 v240, v243, v75
	v_fmac_f32_e32 v240, v242, v74
	v_mul_f32_e32 v193, v243, v39
	v_add_f32_e32 v240, v241, v240
	v_fmac_f32_e32 v193, v242, v38
	v_add_f32_e32 v191, v191, v240
	v_add_f32_e32 v192, v192, v193
	v_add_f32_e32 v105, v105, v192
	s_waitcnt lgkmcnt(4)
	v_mul_f32_e32 v192, v237, v33
	v_mul_f32_e32 v237, v237, v65
	v_fmac_f32_e32 v192, v236, v32
	v_fmac_f32_e32 v237, v236, v64
	v_mul_f32_e32 v236, v239, v63
	v_fmac_f32_e32 v236, v238, v62
	v_mul_f32_e32 v193, v239, v31
	v_add_f32_e32 v236, v237, v236
	v_fmac_f32_e32 v193, v238, v30
	v_add_f32_e32 v191, v191, v236
	v_add_f32_e32 v192, v192, v193
	v_add_f32_e32 v105, v105, v192
	s_waitcnt lgkmcnt(3)
	v_mul_f32_e32 v192, v233, v37
	v_mul_f32_e32 v233, v233, v69
	v_fmac_f32_e32 v192, v232, v36
	v_fmac_f32_e32 v233, v232, v68
	v_mul_f32_e32 v232, v235, v67
	v_fmac_f32_e32 v232, v234, v66
	v_mul_f32_e32 v193, v235, v35
	v_add_f32_e32 v232, v233, v232
	v_fmac_f32_e32 v193, v234, v34
	v_add_f32_e32 v191, v191, v232
	v_add_f32_e32 v192, v192, v193
	v_add_f32_e32 v105, v105, v192
	s_waitcnt lgkmcnt(2)
	v_mul_f32_e32 v192, v229, v29
	v_mul_f32_e32 v229, v229, v61
	v_fmac_f32_e32 v192, v228, v28
	v_fmac_f32_e32 v229, v228, v60
	v_mul_f32_e32 v228, v231, v59
	v_fmac_f32_e32 v228, v230, v58
	v_mul_f32_e32 v193, v231, v27
	v_add_f32_e32 v228, v229, v228
	v_fmac_f32_e32 v193, v230, v26
	v_add_f32_e32 v191, v191, v228
	v_add_f32_e32 v192, v192, v193
	v_add_f32_e32 v105, v105, v192
	s_waitcnt lgkmcnt(1)
	v_mul_f32_e32 v192, v225, v25
	v_mul_f32_e32 v225, v225, v57
	v_fmac_f32_e32 v192, v224, v24
	v_fmac_f32_e32 v225, v224, v56
	v_mul_f32_e32 v224, v227, v55
	v_fmac_f32_e32 v224, v226, v54
	v_mul_f32_e32 v193, v227, v23
	v_add_f32_e32 v224, v225, v224
	v_fmac_f32_e32 v193, v226, v22
	v_add_f32_e32 v191, v191, v224
	v_add_f32_e32 v192, v192, v193
	v_add_f32_e32 v105, v105, v192
	s_waitcnt lgkmcnt(0)
	v_mul_f32_e32 v192, v107, v21
	v_mul_f32_e32 v193, v109, v19
	v_fmac_f32_e32 v192, v106, v20
	v_fmac_f32_e32 v193, v108, v18
	v_add_f32_e32 v192, v192, v193
	v_add_f32_e32 v105, v105, v192
	ds_read_b128 v[192:195], v173
	v_mul_f32_e32 v107, v107, v53
	v_fmac_f32_e32 v107, v106, v52
	v_mul_f32_e32 v106, v109, v51
	v_fmac_f32_e32 v106, v108, v50
	s_waitcnt lgkmcnt(0)
	v_mul_f32_e32 v49, v193, v49
	v_mul_f32_e32 v47, v195, v47
	v_fmac_f32_e32 v49, v192, v48
	v_fmac_f32_e32 v47, v194, v46
	v_add_f32_e32 v46, v49, v47
	v_add_f32_e32 v106, v107, v106
	v_add_f32_e32 v107, 0, v46
	v_mul_f32_e32 v46, v193, v73
	v_mul_f32_e32 v47, v195, v71
	v_fmac_f32_e32 v46, v192, v72
	v_fmac_f32_e32 v47, v194, v70
	v_add_f32_e32 v46, v46, v47
	v_add_f32_e32 v70, 0, v46
	ds_read_b128 v[46:49], v174
	v_add_f32_e32 v106, v191, v106
	s_waitcnt lgkmcnt(0)
	v_mul_f32_e32 v45, v47, v45
	v_mul_f32_e32 v43, v49, v43
	v_fmac_f32_e32 v45, v46, v44
	v_fmac_f32_e32 v43, v48, v42
	v_add_f32_e32 v42, v45, v43
	v_add_f32_e32 v71, v107, v42
	v_mul_f32_e32 v42, v47, v81
	v_mul_f32_e32 v43, v49, v79
	v_fmac_f32_e32 v42, v46, v80
	v_fmac_f32_e32 v43, v48, v78
	v_add_f32_e32 v42, v42, v43
	v_add_f32_e32 v46, v70, v42
	ds_read_b128 v[42:45], v175
	s_waitcnt lgkmcnt(0)
	v_mul_f32_e32 v41, v43, v41
	v_mul_f32_e32 v39, v45, v39
	v_fmac_f32_e32 v41, v42, v40
	v_fmac_f32_e32 v39, v44, v38
	v_add_f32_e32 v38, v41, v39
	v_add_f32_e32 v47, v71, v38
	v_mul_f32_e32 v38, v43, v77
	v_mul_f32_e32 v39, v45, v75
	v_fmac_f32_e32 v38, v42, v76
	v_fmac_f32_e32 v39, v44, v74
	v_add_f32_e32 v38, v38, v39
	v_add_f32_e32 v42, v46, v38
	ds_read_b128 v[38:41], v176
	s_waitcnt lgkmcnt(0)
	v_mul_f32_e32 v33, v39, v33
	v_mul_f32_e32 v31, v41, v31
	v_fmac_f32_e32 v33, v38, v32
	v_fmac_f32_e32 v31, v40, v30
	v_add_f32_e32 v30, v33, v31
	v_add_f32_e32 v43, v47, v30
	v_mul_f32_e32 v30, v39, v65
	v_mul_f32_e32 v31, v41, v63
	v_fmac_f32_e32 v30, v38, v64
	v_fmac_f32_e32 v31, v40, v62
	v_add_f32_e32 v30, v30, v31
	v_add_f32_e32 v38, v42, v30
	ds_read_b128 v[224:227], v177
	ds_read_b128 v[30:33], v178
	s_waitcnt lgkmcnt(1)
	v_mul_f32_e32 v37, v225, v37
	v_mul_f32_e32 v225, v225, v69
	v_fmac_f32_e32 v37, v224, v36
	v_fmac_f32_e32 v225, v224, v68
	v_mul_f32_e32 v224, v227, v67
	v_mul_f32_e32 v35, v227, v35
	v_fmac_f32_e32 v224, v226, v66
	v_fmac_f32_e32 v35, v226, v34
	v_add_f32_e32 v224, v225, v224
	v_add_f32_e32 v34, v37, v35
	v_add_f32_e32 v35, v38, v224
	v_add_f32_e32 v34, v43, v34
	s_waitcnt lgkmcnt(0)
	v_mul_f32_e32 v29, v31, v29
	v_mul_f32_e32 v27, v33, v27
	v_fmac_f32_e32 v29, v30, v28
	v_fmac_f32_e32 v27, v32, v26
	v_add_f32_e32 v26, v29, v27
	v_add_f32_e32 v34, v34, v26
	v_mul_f32_e32 v26, v31, v61
	v_mul_f32_e32 v27, v33, v59
	v_fmac_f32_e32 v26, v30, v60
	v_fmac_f32_e32 v27, v32, v58
	v_add_f32_e32 v26, v26, v27
	v_add_f32_e32 v30, v35, v26
	ds_read_b128 v[26:29], v179
	s_waitcnt lgkmcnt(0)
	v_mul_f32_e32 v25, v27, v25
	v_mul_f32_e32 v23, v29, v23
	v_fmac_f32_e32 v25, v26, v24
	v_fmac_f32_e32 v23, v28, v22
	v_add_f32_e32 v22, v25, v23
	v_add_f32_e32 v31, v34, v22
	v_mul_f32_e32 v22, v27, v57
	v_mul_f32_e32 v23, v29, v55
	v_fmac_f32_e32 v22, v26, v56
	v_fmac_f32_e32 v23, v28, v54
	v_add_f32_e32 v22, v22, v23
	v_add_f32_e32 v26, v30, v22
	ds_read_b128 v[22:25], v180
	v_cndmask_b32_e64 v27, v92, v104, s[34:35]
	v_cndmask_b32_e64 v28, v104, v92, s[34:35]
	v_cndmask_b32_e64 v29, v94, v106, s[34:35]
	v_cndmask_b32_e64 v30, v106, v94, s[34:35]
	s_waitcnt lgkmcnt(0)
	v_mul_f32_e32 v21, v23, v21
	v_mul_f32_e32 v19, v25, v19
	v_fmac_f32_e32 v21, v22, v20
	v_fmac_f32_e32 v19, v24, v18
	v_add_f32_e32 v18, v21, v19
	v_mul_f32_e32 v19, v23, v53
	v_mul_f32_e32 v20, v25, v51
	v_fmac_f32_e32 v19, v22, v52
	v_fmac_f32_e32 v20, v24, v50
	v_add_f32_e32 v19, v19, v20
	v_cndmask_b32_e64 v20, v2, v4, s[34:35]
	v_cndmask_b32_e64 v2, v4, v2, s[34:35]
	v_cndmask_b32_e64 v4, v82, v5, s[34:35]
	ds_bpermute_b32 v4, v112, v4
	v_cndmask_b32_e64 v5, v5, v82, s[34:35]
	ds_bpermute_b32 v20, v112, v20
	v_cndmask_b32_e64 v21, v86, v98, s[34:35]
	v_cndmask_b32_e64 v22, v98, v86, s[34:35]
	s_waitcnt lgkmcnt(1)
	v_add_f32_e32 v4, v5, v4
	v_cndmask_b32_e64 v5, v83, v6, s[34:35]
	ds_bpermute_b32 v5, v112, v5
	s_waitcnt lgkmcnt(1)
	v_add_f32_e32 v2, v2, v20
	v_cndmask_b32_e64 v6, v6, v83, s[34:35]
	v_cndmask_b32_e64 v20, v84, v7, s[34:35]
	v_cndmask_b32_e64 v7, v7, v84, s[34:35]
	s_waitcnt lgkmcnt(0)
	v_add_f32_e32 v5, v6, v5
	ds_bpermute_b32 v6, v112, v20
	v_cndmask_b32_e64 v20, v97, v85, s[34:35]
	v_cndmask_b32_e64 v23, v88, v100, s[34:35]
	v_cndmask_b32_e64 v24, v100, v88, s[34:35]
	v_cndmask_b32_e64 v25, v90, v102, s[34:35]
	s_waitcnt lgkmcnt(0)
	v_add_f32_e32 v6, v7, v6
	v_cndmask_b32_e64 v7, v85, v97, s[34:35]
	ds_bpermute_b32 v7, v112, v7
	v_add_f32_e32 v19, v26, v19
	v_cndmask_b32_e64 v26, v102, v90, s[34:35]
	v_add_f32_e32 v18, v31, v18
	s_waitcnt lgkmcnt(0)
	v_add_f32_e32 v7, v20, v7
	ds_bpermute_b32 v20, v112, v21
	v_cndmask_b32_e64 v21, v87, v99, s[34:35]
	ds_bpermute_b32 v21, v112, v21
	s_waitcnt lgkmcnt(1)
	v_add_f32_e32 v20, v22, v20
	v_cndmask_b32_e64 v22, v99, v87, s[34:35]
	s_waitcnt lgkmcnt(0)
	v_add_f32_e32 v21, v22, v21
	ds_bpermute_b32 v22, v112, v23
	v_cndmask_b32_e64 v23, v89, v101, s[34:35]
	ds_bpermute_b32 v23, v112, v23
	s_waitcnt lgkmcnt(1)
	v_add_f32_e32 v22, v24, v22
	v_cndmask_b32_e64 v24, v101, v89, s[34:35]
	s_waitcnt lgkmcnt(0)
	v_add_f32_e32 v23, v24, v23
	ds_bpermute_b32 v24, v112, v25
	v_cndmask_b32_e64 v25, v91, v103, s[34:35]
	ds_bpermute_b32 v25, v112, v25
	s_waitcnt lgkmcnt(1)
	v_add_f32_e32 v24, v26, v24
	v_cndmask_b32_e64 v26, v103, v91, s[34:35]
	s_waitcnt lgkmcnt(0)
	v_add_f32_e32 v25, v26, v25
	ds_bpermute_b32 v26, v112, v27
	v_cndmask_b32_e64 v27, v93, v105, s[34:35]
	ds_bpermute_b32 v27, v112, v27
	s_waitcnt lgkmcnt(1)
	v_add_f32_e32 v26, v28, v26
	v_cndmask_b32_e64 v28, v105, v93, s[34:35]
	s_waitcnt lgkmcnt(0)
	v_add_f32_e32 v27, v28, v27
	ds_bpermute_b32 v28, v112, v29
	v_cndmask_b32_e64 v29, v95, v18, s[34:35]
	ds_bpermute_b32 v29, v112, v29
	v_cndmask_b32_e64 v18, v18, v95, s[34:35]
	s_waitcnt lgkmcnt(1)
	v_add_f32_e32 v28, v30, v28
	v_cndmask_b32_e64 v30, v96, v19, s[34:35]
	s_waitcnt lgkmcnt(0)
	v_add_f32_e32 v18, v18, v29
	ds_bpermute_b32 v29, v112, v30
	v_cndmask_b32_e64 v19, v19, v96, s[34:35]
	s_waitcnt lgkmcnt(0)
	v_add_f32_e32 v19, v19, v29
	v_cndmask_b32_e64 v29, v2, v23, s[36:37]
	v_cndmask_b32_e64 v2, v23, v2, s[36:37]
	v_cndmask_b32_e64 v23, v4, v24, s[36:37]
	ds_bpermute_b32 v23, v111, v23
	v_cndmask_b32_e64 v4, v24, v4, s[36:37]
	ds_bpermute_b32 v24, v111, v29
	s_waitcnt lgkmcnt(1)
	v_add_f32_e32 v4, v4, v23
	v_cndmask_b32_e64 v23, v5, v25, s[36:37]
	ds_bpermute_b32 v23, v111, v23
	s_waitcnt lgkmcnt(1)
	v_add_f32_e32 v2, v2, v24
	v_cndmask_b32_e64 v5, v25, v5, s[36:37]
	v_cndmask_b32_e64 v24, v6, v26, s[36:37]
	v_cndmask_b32_e64 v6, v26, v6, s[36:37]
	s_waitcnt lgkmcnt(0)
	v_add_f32_e32 v5, v5, v23
	ds_bpermute_b32 v23, v111, v24
	v_cndmask_b32_e64 v24, v20, v28, s[36:37]
	v_cndmask_b32_e64 v20, v28, v20, s[36:37]
	s_waitcnt lgkmcnt(0)
	v_add_f32_e32 v6, v6, v23
	v_cndmask_b32_e64 v23, v7, v27, s[36:37]
	ds_bpermute_b32 v23, v111, v23
	v_cndmask_b32_e64 v7, v27, v7, s[36:37]
	s_waitcnt lgkmcnt(0)
	v_add_f32_e32 v7, v7, v23
	ds_bpermute_b32 v23, v111, v24
	s_waitcnt lgkmcnt(0)
	v_add_f32_e32 v20, v20, v23
	v_cndmask_b32_e64 v23, v21, v18, s[36:37]
	v_cndmask_b32_e64 v18, v18, v21, s[36:37]
	v_cndmask_b32_e64 v21, v22, v19, s[36:37]
	ds_bpermute_b32 v21, v111, v21
	v_cndmask_b32_e64 v19, v19, v22, s[36:37]
	ds_bpermute_b32 v22, v111, v23
	s_waitcnt lgkmcnt(1)
	v_add_f32_e32 v19, v19, v21
	v_cndmask_b32_e64 v21, v2, v7, s[38:39]
	v_cndmask_b32_e64 v2, v7, v2, s[38:39]
	v_cndmask_b32_e64 v7, v4, v20, s[38:39]
	ds_bpermute_b32 v7, v113, v7
	s_waitcnt lgkmcnt(1)
	v_add_f32_e32 v18, v18, v22
	v_cndmask_b32_e64 v4, v20, v4, s[38:39]
	ds_bpermute_b32 v20, v113, v21
	s_waitcnt lgkmcnt(1)
	v_add_f32_e32 v4, v4, v7
	v_cndmask_b32_e64 v7, v5, v18, s[38:39]
	ds_bpermute_b32 v7, v113, v7
	v_cndmask_b32_e64 v5, v18, v5, s[38:39]
	v_cndmask_b32_e64 v18, v6, v19, s[38:39]
	s_waitcnt lgkmcnt(1)
	v_add_f32_e32 v2, v2, v20
	v_cndmask_b32_e64 v6, v19, v6, s[38:39]
	s_waitcnt lgkmcnt(0)
	v_add_f32_e32 v5, v5, v7
	ds_bpermute_b32 v7, v113, v18
	s_waitcnt lgkmcnt(0)
	v_add_f32_e32 v6, v6, v7
	v_cndmask_b32_e64 v7, v2, v5, s[40:41]
	v_cndmask_b32_e64 v2, v5, v2, s[40:41]
	v_cndmask_b32_e64 v5, v4, v6, s[40:41]
	v_cndmask_b32_e64 v4, v6, v4, s[40:41]
	ds_bpermute_b32 v6, v114, v7
	ds_bpermute_b32 v5, v114, v5
	s_waitcnt lgkmcnt(1)
	v_add_f32_e32 v2, v2, v6
	s_waitcnt lgkmcnt(0)
	v_add_f32_e32 v4, v4, v5
	ds_bpermute_b32 v5, v115, v2
	s_waitcnt lgkmcnt(0)
	v_add_f32_e32 v2, v2, v5
	ds_bpermute_b32 v5, v115, v4
	s_waitcnt lgkmcnt(0)
	v_add_f32_e32 v4, v4, v5
	ds_bpermute_b32 v5, v116, v2
	s_waitcnt lgkmcnt(0)
	v_add_f32_e32 v2, v2, v5
	ds_bpermute_b32 v5, v116, v4
	s_waitcnt lgkmcnt(0)
	v_add_f32_e32 v5, v4, v5
	ds_bpermute_b32 v4, v114, v2
	ds_bpermute_b32 v6, v114, v5
	s_waitcnt lgkmcnt(1)
	v_max_f32_e32 v4, v4, v4
	v_max_f32_e32 v4, v2, v4
	ds_bpermute_b32 v7, v113, v4
	s_waitcnt lgkmcnt(1)
	v_max_f32_e32 v6, v6, v6
	v_max_f32_e32 v6, v5, v6
	s_waitcnt lgkmcnt(0)
	v_max_f32_e32 v7, v7, v7
	v_max_f32_e32 v4, v4, v7
	ds_bpermute_b32 v7, v113, v6
	s_waitcnt lgkmcnt(0)
	v_max_f32_e32 v7, v7, v7
	v_max_f32_e32 v6, v6, v7
	ds_bpermute_b32 v7, v111, v4
	s_waitcnt lgkmcnt(0)
	v_max_f32_e32 v7, v7, v7
	v_max_f32_e32 v4, v4, v7
	ds_bpermute_b32 v7, v111, v6
	s_waitcnt lgkmcnt(0)
	v_max_f32_e32 v7, v7, v7
	v_max_f32_e32 v6, v6, v7
	ds_bpermute_b32 v7, v112, v4
	s_waitcnt lgkmcnt(0)
	v_max_f32_e32 v7, v7, v7
	v_max_f32_e32 v4, v4, v7
	ds_bpermute_b32 v7, v112, v6
	v_sub_f32_e32 v2, v2, v4
	v_mul_f32_e32 v2, 0x3fb8aa3b, v2
	v_exp_f32_e32 v4, v2
	s_waitcnt lgkmcnt(0)
	v_max_f32_e32 v7, v7, v7
	v_max_f32_e32 v6, v6, v7
	v_sub_f32_e32 v2, v5, v6
	v_mul_f32_e32 v2, 0x3fb8aa3b, v2
	ds_bpermute_b32 v5, v114, v4
	v_exp_f32_e32 v2, v2
	s_waitcnt lgkmcnt(0)
	v_add_f32_e32 v5, v4, v5
	ds_bpermute_b32 v6, v114, v2
	ds_bpermute_b32 v7, v113, v5
	s_waitcnt lgkmcnt(1)
	v_add_f32_e32 v6, v2, v6
	s_waitcnt lgkmcnt(0)
	v_add_f32_e32 v5, v5, v7
	ds_bpermute_b32 v7, v113, v6
	s_waitcnt lgkmcnt(0)
	v_add_f32_e32 v6, v6, v7
	ds_bpermute_b32 v7, v111, v5
	s_waitcnt lgkmcnt(0)
	v_add_f32_e32 v7, v5, v7
	ds_bpermute_b32 v5, v111, v6
	ds_bpermute_b32 v18, v112, v7
	s_waitcnt lgkmcnt(1)
	v_add_f32_e32 v5, v6, v5
	ds_bpermute_b32 v6, v112, v5
	s_and_saveexec_b64 s[0:1], s[42:43]
	s_cbranch_execz .LBB0_2122
	s_waitcnt lgkmcnt(1)
	v_add_f32_e32 v7, v7, v18
	v_div_scale_f32 v18, s[2:3], v7, v7, v4
	v_rcp_f32_e32 v19, v18
	v_div_scale_f32 v20, vcc, v4, v7, v4
	s_cmp_eq_u32 s8, s48
	v_fma_f32 v21, -v18, v19, 1.0
	v_fmac_f32_e32 v19, v21, v19
	v_mul_f32_e32 v21, v20, v19
	v_fma_f32 v22, -v18, v21, v20
	v_fmac_f32_e32 v21, v22, v19
	v_fma_f32 v18, -v18, v21, v20
	v_div_fmas_f32 v18, v18, v19, v21
	v_div_fixup_f32 v4, v18, v7, v4
	v_lshl_add_u64 v[18:19], s[44:45], 0, v[14:15]
	global_store_dword v[18:19], v4, off
	s_cbranch_scc1 .LBB0_2122
	s_waitcnt lgkmcnt(0)
	v_add_f32_e32 v4, v5, v6
	v_div_scale_f32 v5, s[2:3], v4, v4, v2
	v_rcp_f32_e32 v6, v5
	v_div_scale_f32 v7, vcc, v2, v4, v2
	s_lshl_b64 s[2:3], s[48:49], 6
	v_fma_f32 v18, -v5, v6, 1.0
	v_fmac_f32_e32 v6, v18, v6
	v_mul_f32_e32 v18, v7, v6
	v_fma_f32 v19, -v5, v18, v7
	v_fmac_f32_e32 v18, v19, v6
	v_fma_f32 v5, -v5, v18, v7
	v_div_fmas_f32 v5, v5, v6, v18
	v_div_fixup_f32 v2, v5, v4, v2
	v_lshl_add_u64 v[4:5], v[10:11], 0, s[2:3]
	global_store_dword v[4:5], v2, off
	s_branch .LBB0_2122
